# v53 + both G1 epilogues two-stage rstd8: five of eight rows' SS partial-sum loads prefetched at unit top into spare VGPRs, last three loaded right after the K loop and consumed after five row blocks
# baseline (speedup 1.0000x reference)
; #define PG8_STAGE_A(b, h, ptr, NX) do { if constexpr (Sched::GATHER) { unsigned gs_[2]; gs_[0] = ((NX) && last_) ? gN[h][0] : gA[h][0]; gs_[1] = ((NX) && last_) ? gN[h][1] : gA[h][1]; PG8_STAGE(PG8_SA(b, h), ptr, gs_); } \
;         else PG8_STAGE(PG8_SA(b, h), (ptr) + ((h) ? hstep : (size_t)0), voffA); } while (0)
; #define PG8_STAGE(bufoff, gbase, voff) do { _Pragma("unroll") for (int _i = 0; _i < 2; ++_i) \
;         __builtin_amdgcn_global_load_lds((const unsigned*)((const char*)(gbase) + (voff)[_i]), (PG8_LAS unsigned*)(lds + (bufoff) + ldsw + _i * 8192), 16, 0, 0); } while (0)
; #define PG8_LDA(dst, b, h) do { _Pragma("unroll") for (int m = 0; m < 4; ++m) _Pragma("unroll") for (int k = 0; k < 2; ++k) dst[m][k] = *(const PG8_LAS bf16x8*)(lds + PG8_SA(b, h) + aoff + m * 2048 + k * 1024); } while (0)
; #define PG8_LDB(dst, b, h) do { _Pragma("unroll") for (int n = 0; n < 2; ++n) _Pragma("unroll") for (int k = 0; k < 2; ++k) dst[n][k] = *(const PG8_LAS bf16x8*)(lds + PG8_SB(b, h) + boff + n * 2048 + k * 1024); } while (0)
; #define PG8_WAIT_V(n) asm volatile("s_waitcnt vmcnt(" #n ")" ::: "memory")
; #define PG8_WAIT_L(n) asm volatile("s_waitcnt lgkmcnt(" #n ")" ::: "memory")
; #define PG8_BAR __builtin_amdgcn_s_barrier()
; #define PG8_SCHED __builtin_amdgcn_sched_barrier(0)
; __device__ __forceinline__ void rstd8(const float* SS, int rowb, int lane, float (&rs)[2][4]) {
;     f32x4 p[2][4];
; #pragma unroll
;     for (int ai = 0; ai < 2; ++ai)
; #pragma unroll
;         for (int m = 0; m < 4; ++m) p[ai][m] = *(const f32x4*)(SS + (size_t)(rowb + HALF * ai + 16 * m + (lane >> 2)) * 16 + 4 * (lane & 3));
; template <class Epi, class Sched, bool ALIGN_EPI = false, bool SP2 = false>
; __device__ __forceinline__ void gemm_phase(PG8_LAS unsigned char* lds, const Gemm g, const Sched& S, const Epi& E, const bool skip_epi = false) {
;     ...
;             PG8_LDB(B0, 0, 0); PG8_LDB(B1, 0, 1); PG8_SCHED; PG8_LDA(At, 0, 0); PG8_STAGE_A(1, 1, a1, false);
;             PG8_WAIT_V(8); PG8_WAIT_L(0); PG8_BAR; PG8_MMA(0, 0, At, B0); PG8_MMA(0, 1, At, B1); PG8_BAR; PG8_SCHED;
;             PG8_LDA(At, 0, 1); PG8_STAGE(PG8_SB(0, 0), b2, voffB); PG8_STAGE(PG8_SB(0, 1), b2 + hstep, voffB); PG8_STAGE_A(0, 0, a2, true);
;             PG8_WAIT_V(8); PG8_WAIT_L(0); PG8_BAR; PG8_MMA(1, 0, At, B0); PG8_MMA(1, 1, At, B1); PG8_BAR; PG8_SCHED;
.LBB0_252:
	s_ashr_i32 s17, s16, 31
	s_lshl_b64 s[18:19], s[16:17], 19
	s_add_u32 s18, s86, s18
	s_addc_u32 s19, s87, s19
	s_and_b64 s[20:21], s[4:5], exec
	s_cselect_b32 s17, s19, s25
	s_cselect_b32 s56, s18, s24
	s_ashr_i32 s15, s14, 31
	s_lshl_b64 s[20:21], s[14:15], 19
	v_readlane_b32 s28, v254, 36
	v_readlane_b32 s29, v254, 37
	s_add_u32 s20, s28, s20
	s_addc_u32 s21, s29, s21
	s_and_b64 s[28:29], s[4:5], exec
	s_cselect_b32 s15, s21, s27
	s_cselect_b32 s57, s20, s26
	s_add_u32 s24, s24, 0x40080
	s_addc_u32 s25, s25, 0
	s_add_u32 s58, s26, 0x100
	s_addc_u32 s59, s27, 0
	s_mov_b32 s60, -2
	s_waitcnt vmcnt(0)
	v_lshl_add_u32 v148, s22, 8, v167
	v_ashrrev_i32_e32 v149, 31, v148
	v_lshlrev_b64 v[148:149], 6, v[148:149]
	v_lshl_add_u64 v[148:149], v[138:139], 0, v[148:149]
	v_add_co_u32_e32 v150, vcc, 0x2000, v148
	v_addc_co_u32_e32 v151, vcc, 0, v149, vcc
	global_load_dwordx4 v[234:237], v[148:149], off
	global_load_dwordx4 v[238:241], v[148:149], off offset:1024
	global_load_dwordx4 v[242:245], v[148:149], off offset:2048
	global_load_dwordx4 v[246:249], v[148:149], off offset:3072
	global_load_dwordx4 v[250:253], v[150:151], off
	ds_read_b128 v[148:151], v170
	ds_read_b128 v[152:155], v170 offset:1024
	ds_read_b128 v[156:159], v170 offset:2048
	ds_read_b128 v[160:163], v170 offset:3072
	ds_read_b128 v[176:179], v171
	ds_read_b128 v[180:183], v171 offset:1024
	ds_read_b128 v[184:187], v171 offset:2048
	ds_read_b128 v[188:191], v171 offset:3072
	s_add_u32 s26, s24, 0xfffc0080
	s_addc_u32 s27, s25, -1
	s_cmp_eq_u32 s60, 12
	s_cselect_b32 s29, s17, s27
	s_cselect_b32 s28, s56, s26
	s_cselect_b32 s27, s15, s59
	s_cselect_b32 s26, s57, s58
	v_lshl_add_u64 v[164:165], s[24:25], 0, v[140:141]
	s_add_i32 m0, s23, 0xc000
	ds_read_b128 v[192:195], v172
	ds_read_b128 v[196:199], v172 offset:1024
	ds_read_b128 v[200:203], v172 offset:2048
	ds_read_b128 v[204:207], v172 offset:3072
	ds_read_b128 v[208:211], v172 offset:4096
	ds_read_b128 v[212:215], v172 offset:5120
	ds_read_b128 v[216:219], v172 offset:6144
	ds_read_b128 v[220:223], v172 offset:7168
	global_load_lds_dwordx4 v[164:165], off
	v_lshl_add_u64 v[164:165], s[24:25], 0, v[142:143]
	s_add_i32 m0, s23, 0xe000
	s_nop 0
	global_load_lds_dwordx4 v[164:165], off
	s_waitcnt vmcnt(8)
	s_waitcnt lgkmcnt(0)
	s_barrier
	s_setprio 1
	s_waitcnt lgkmcnt(0)
	v_mfma_f32_16x16x32_bf16 v[126:129], v[148:151], v[192:195], 0
	v_mfma_f32_16x16x32_bf16 v[122:125], v[156:159], v[192:195], 0
	v_mfma_f32_16x16x32_bf16 v[114:117], v[148:151], v[200:203], 0
	v_mfma_f32_16x16x32_bf16 v[106:109], v[156:159], v[200:203], 0
	v_mfma_f32_16x16x32_bf16 v[98:101], v[148:151], v[208:211], 0
	v_mfma_f32_16x16x32_bf16 v[90:93], v[156:159], v[208:211], 0
	v_mfma_f32_16x16x32_bf16 v[82:85], v[148:151], v[216:219], 0
	v_mfma_f32_16x16x32_bf16 v[74:77], v[156:159], v[216:219], 0
	v_mfma_f32_16x16x32_bf16 v[126:129], v[152:155], v[196:199], v[126:129]
	v_mfma_f32_16x16x32_bf16 v[122:125], v[160:163], v[196:199], v[122:125]
	v_mfma_f32_16x16x32_bf16 v[114:117], v[152:155], v[204:207], v[114:117]
	v_mfma_f32_16x16x32_bf16 v[106:109], v[160:163], v[204:207], v[106:109]
	v_mfma_f32_16x16x32_bf16 v[98:101], v[152:155], v[212:215], v[98:101]
	v_mfma_f32_16x16x32_bf16 v[90:93], v[160:163], v[212:215], v[90:93]
	v_mfma_f32_16x16x32_bf16 v[82:85], v[152:155], v[220:223], v[82:85]
	v_mfma_f32_16x16x32_bf16 v[74:77], v[160:163], v[220:223], v[74:77]
	s_setprio 0
	s_setprio 1
	v_mfma_f32_16x16x32_bf16 v[118:121], v[176:179], v[192:195], 0
	v_mfma_f32_16x16x32_bf16 v[110:113], v[184:187], v[192:195], 0
	v_mfma_f32_16x16x32_bf16 v[102:105], v[176:179], v[200:203], 0
	v_mfma_f32_16x16x32_bf16 v[94:97], v[184:187], v[200:203], 0
	v_mfma_f32_16x16x32_bf16 v[86:89], v[176:179], v[208:211], 0
	v_mfma_f32_16x16x32_bf16 v[78:81], v[184:187], v[208:211], 0
	v_mfma_f32_16x16x32_bf16 v[70:73], v[176:179], v[216:219], 0
	v_mfma_f32_16x16x32_bf16 v[66:69], v[184:187], v[216:219], 0
	v_mfma_f32_16x16x32_bf16 v[118:121], v[180:183], v[196:199], v[118:121]
	v_mfma_f32_16x16x32_bf16 v[110:113], v[188:191], v[196:199], v[110:113]
	v_mfma_f32_16x16x32_bf16 v[102:105], v[180:183], v[204:207], v[102:105]
	v_mfma_f32_16x16x32_bf16 v[94:97], v[188:191], v[204:207], v[94:97]
	v_mfma_f32_16x16x32_bf16 v[86:89], v[180:183], v[212:215], v[86:89]
	v_mfma_f32_16x16x32_bf16 v[78:81], v[188:191], v[212:215], v[78:81]
	v_mfma_f32_16x16x32_bf16 v[70:73], v[180:183], v[220:223], v[70:73]
	v_mfma_f32_16x16x32_bf16 v[66:69], v[188:191], v[220:223], v[66:69]
	s_setprio 0
	s_barrier
	s_add_i32 s61, s46, s2
	v_lshl_add_u64 v[164:165], s[26:27], 0, v[134:135]
	s_mov_b32 m0, s61
	ds_read_b128 v[192:195], v172 offset:16384
	ds_read_b128 v[196:199], v172 offset:17408
	ds_read_b128 v[200:203], v172 offset:18432
	ds_read_b128 v[204:207], v172 offset:19456
	ds_read_b128 v[208:211], v172 offset:20480
	ds_read_b128 v[212:215], v172 offset:21504
	ds_read_b128 v[216:219], v172 offset:22528
	ds_read_b128 v[220:223], v172 offset:23552
	global_load_lds_dwordx4 v[164:165], off
	s_add_i32 m0, s61, 0x2000
	s_add_u32 s62, s26, 0x40000
	v_lshl_add_u64 v[224:225], s[26:27], 0, v[130:131]
	s_addc_u32 s63, s27, 0
	s_add_i32 s61, s47, s2
	global_load_lds_dwordx4 v[224:225], off
	v_lshl_add_u64 v[226:227], s[62:63], 0, v[134:135]
	s_mov_b32 m0, s61
	v_lshl_add_u64 v[230:231], s[28:29], 0, v[132:133]
	global_load_lds_dwordx4 v[226:227], off
	v_lshl_add_u64 v[226:227], s[62:63], 0, v[130:131]
	s_add_i32 m0, s61, 0x2000
	s_nop 0
	global_load_lds_dwordx4 v[226:227], off
	v_lshl_add_u64 v[226:227], s[28:29], 0, v[136:137]
	s_mov_b32 m0, s23
	s_nop 0
	global_load_lds_dwordx4 v[226:227], off
	s_mov_b32 m0, s31
	s_nop 0
	global_load_lds_dwordx4 v[230:231], off
	s_waitcnt vmcnt(8)
	s_waitcnt lgkmcnt(0)
	s_barrier
; #define PG8_STAGE_A(b, h, ptr, NX) do { if constexpr (Sched::GATHER) { unsigned gs_[2]; gs_[0] = ((NX) && last_) ? gN[h][0] : gA[h][0]; gs_[1] = ((NX) && last_) ? gN[h][1] : gA[h][1]; PG8_STAGE(PG8_SA(b, h), ptr, gs_); } \
;         else PG8_STAGE(PG8_SA(b, h), (ptr) + ((h) ? hstep : (size_t)0), voffA); } while (0)
; #define PG8_STAGE(bufoff, gbase, voff) do { _Pragma("unroll") for (int _i = 0; _i < 2; ++_i) \
;         __builtin_amdgcn_global_load_lds((const unsigned*)((const char*)(gbase) + (voff)[_i]), (PG8_LAS unsigned*)(lds + (bufoff) + ldsw + _i * 8192), 16, 0, 0); } while (0)
; #define PG8_LDA(dst, b, h) do { _Pragma("unroll") for (int m = 0; m < 4; ++m) _Pragma("unroll") for (int k = 0; k < 2; ++k) dst[m][k] = *(const PG8_LAS bf16x8*)(lds + PG8_SA(b, h) + aoff + m * 2048 + k * 1024); } while (0)
; #define PG8_LDB(dst, b, h) do { _Pragma("unroll") for (int n = 0; n < 2; ++n) _Pragma("unroll") for (int k = 0; k < 2; ++k) dst[n][k] = *(const PG8_LAS bf16x8*)(lds + PG8_SB(b, h) + boff + n * 2048 + k * 1024); } while (0)
; #define PG8_MMA(ai, bj, At, Bt) do { __builtin_amdgcn_s_setprio(1); _Pragma("unroll") for (int m = 0; m < 4; ++m) _Pragma("unroll") for (int n = 0; n < 2; ++n) _Pragma("unroll") for (int k = 0; k < 2; ++k) \
;         acc[ai][bj][m][n] = __builtin_amdgcn_mfma_f32_16x16x32_bf16(Bt[n][k], At[m][k], acc[ai][bj][m][n], 0, 0, 0); __builtin_amdgcn_s_setprio(0); } while (0)
; #define PG8_WAIT_V(n) asm volatile("s_waitcnt vmcnt(" #n ")" ::: "memory")
; #define PG8_WAIT_L(n) asm volatile("s_waitcnt lgkmcnt(" #n ")" ::: "memory")
; #define PG8_BAR __builtin_amdgcn_s_barrier()
; #define PG8_SCHED __builtin_amdgcn_sched_barrier(0)
; template <class Epi, class Sched, bool ALIGN_EPI = false, bool SP2 = false>
; __device__ __forceinline__ void gemm_phase(PG8_LAS unsigned char* lds, const Gemm g, const Sched& S, const Epi& E, const bool skip_epi = false) {
;     ...
;             PG8_WAIT_V(8); PG8_WAIT_L(0); PG8_BAR; PG8_MMA(1, 0, At, B0); PG8_MMA(1, 1, At, B1); PG8_BAR; PG8_SCHED;
;             PG8_LDB(B0, 1, 0); PG8_LDB(B1, 1, 1); PG8_SCHED; PG8_LDA(At, 1, 0); PG8_STAGE_A(0, 1, a2, true);
;             PG8_WAIT_V(8); PG8_WAIT_L(0); PG8_BAR; PG8_MMA(0, 0, At, B0); PG8_MMA(0, 1, At, B1); PG8_BAR; PG8_SCHED;
;             PG8_LDA(At, 1, 1); PG8_STAGE(PG8_SB(1, 0), b3, voffB); PG8_STAGE(PG8_SB(1, 1), b3 + hstep, voffB); PG8_STAGE_A(1, 0, a3, true);
	s_setprio 1
	s_waitcnt lgkmcnt(0)
	v_mfma_f32_16x16x32_bf16 v[62:65], v[148:151], v[192:195], 0
	v_mfma_f32_16x16x32_bf16 v[58:61], v[156:159], v[192:195], 0
	v_mfma_f32_16x16x32_bf16 v[50:53], v[148:151], v[200:203], 0
	v_mfma_f32_16x16x32_bf16 v[42:45], v[156:159], v[200:203], 0
	v_mfma_f32_16x16x32_bf16 v[34:37], v[148:151], v[208:211], 0
	v_mfma_f32_16x16x32_bf16 v[26:29], v[156:159], v[208:211], 0
	v_mfma_f32_16x16x32_bf16 v[18:21], v[148:151], v[216:219], 0
	v_mfma_f32_16x16x32_bf16 v[10:13], v[156:159], v[216:219], 0
	v_mfma_f32_16x16x32_bf16 v[62:65], v[152:155], v[196:199], v[62:65]
	v_mfma_f32_16x16x32_bf16 v[58:61], v[160:163], v[196:199], v[58:61]
	v_mfma_f32_16x16x32_bf16 v[50:53], v[152:155], v[204:207], v[50:53]
	v_mfma_f32_16x16x32_bf16 v[42:45], v[160:163], v[204:207], v[42:45]
	v_mfma_f32_16x16x32_bf16 v[34:37], v[152:155], v[212:215], v[34:37]
	v_mfma_f32_16x16x32_bf16 v[26:29], v[160:163], v[212:215], v[26:29]
	v_mfma_f32_16x16x32_bf16 v[18:21], v[152:155], v[220:223], v[18:21]
	v_mfma_f32_16x16x32_bf16 v[10:13], v[160:163], v[220:223], v[10:13]
	s_setprio 0
	s_setprio 1
	v_mfma_f32_16x16x32_bf16 v[54:57], v[176:179], v[192:195], 0
	v_mfma_f32_16x16x32_bf16 v[46:49], v[184:187], v[192:195], 0
	v_mfma_f32_16x16x32_bf16 v[38:41], v[176:179], v[200:203], 0
	v_mfma_f32_16x16x32_bf16 v[30:33], v[184:187], v[200:203], 0
	v_mfma_f32_16x16x32_bf16 v[22:25], v[176:179], v[208:211], 0
	v_mfma_f32_16x16x32_bf16 v[14:17], v[184:187], v[208:211], 0
	v_mfma_f32_16x16x32_bf16 v[6:9], v[176:179], v[216:219], 0
	v_mfma_f32_16x16x32_bf16 v[2:5], v[184:187], v[216:219], 0
	v_mfma_f32_16x16x32_bf16 v[54:57], v[180:183], v[196:199], v[54:57]
	v_mfma_f32_16x16x32_bf16 v[46:49], v[188:191], v[196:199], v[46:49]
	v_mfma_f32_16x16x32_bf16 v[38:41], v[180:183], v[204:207], v[38:41]
	v_mfma_f32_16x16x32_bf16 v[30:33], v[188:191], v[204:207], v[30:33]
	v_mfma_f32_16x16x32_bf16 v[22:25], v[180:183], v[212:215], v[22:25]
	v_mfma_f32_16x16x32_bf16 v[14:17], v[188:191], v[212:215], v[14:17]
	v_mfma_f32_16x16x32_bf16 v[6:9], v[180:183], v[220:223], v[6:9]
	v_mfma_f32_16x16x32_bf16 v[2:5], v[188:191], v[220:223], v[2:5]
	s_setprio 0
	s_barrier
	s_add_i32 s61, 0, 0x18000
	s_add_i32 s62, 0, 0x1c000
	v_add_u32_e32 v160, s61, v1
	v_add_u32_e32 v188, s62, v1
	ds_read_b128 v[148:151], v160
	ds_read_b128 v[152:155], v160 offset:1024
	ds_read_b128 v[156:159], v160 offset:2048
	ds_read_b128 v[160:163], v160 offset:3072
	ds_read_b128 v[176:179], v188
	ds_read_b128 v[180:183], v188 offset:1024
	ds_read_b128 v[184:187], v188 offset:2048
	ds_read_b128 v[188:191], v188 offset:3072
	s_add_u32 s28, s28, 0x40000
	s_addc_u32 s29, s29, 0
	s_mov_b32 m0, s34
	v_lshl_add_u64 v[232:233], s[28:29], 0, v[136:137]
	ds_read_b128 v[192:195], v172 offset:32768
	ds_read_b128 v[196:199], v172 offset:33792
	ds_read_b128 v[200:203], v172 offset:34816
	ds_read_b128 v[204:207], v172 offset:35840
	ds_read_b128 v[208:211], v172 offset:36864
	ds_read_b128 v[212:215], v172 offset:37888
	ds_read_b128 v[216:219], v172 offset:38912
	ds_read_b128 v[220:223], v172 offset:39936
	global_load_lds_dwordx4 v[232:233], off
	v_lshl_add_u64 v[232:233], s[28:29], 0, v[132:133]
	s_mov_b32 m0, s35
	s_nop 0
	global_load_lds_dwordx4 v[232:233], off
	s_waitcnt vmcnt(8)
	s_waitcnt lgkmcnt(0)
	s_barrier
	s_setprio 1
	s_waitcnt lgkmcnt(0)
	v_mfma_f32_16x16x32_bf16 v[126:129], v[148:151], v[192:195], v[126:129]
	v_mfma_f32_16x16x32_bf16 v[122:125], v[156:159], v[192:195], v[122:125]
	v_mfma_f32_16x16x32_bf16 v[114:117], v[148:151], v[200:203], v[114:117]
	v_mfma_f32_16x16x32_bf16 v[106:109], v[156:159], v[200:203], v[106:109]
	v_mfma_f32_16x16x32_bf16 v[98:101], v[148:151], v[208:211], v[98:101]
	v_mfma_f32_16x16x32_bf16 v[90:93], v[156:159], v[208:211], v[90:93]
	v_mfma_f32_16x16x32_bf16 v[82:85], v[148:151], v[216:219], v[82:85]
	v_mfma_f32_16x16x32_bf16 v[74:77], v[156:159], v[216:219], v[74:77]
	v_mfma_f32_16x16x32_bf16 v[126:129], v[152:155], v[196:199], v[126:129]
	v_mfma_f32_16x16x32_bf16 v[122:125], v[160:163], v[196:199], v[122:125]
	v_mfma_f32_16x16x32_bf16 v[114:117], v[152:155], v[204:207], v[114:117]
	v_mfma_f32_16x16x32_bf16 v[106:109], v[160:163], v[204:207], v[106:109]
	v_mfma_f32_16x16x32_bf16 v[98:101], v[152:155], v[212:215], v[98:101]
	v_mfma_f32_16x16x32_bf16 v[90:93], v[160:163], v[212:215], v[90:93]
	v_mfma_f32_16x16x32_bf16 v[82:85], v[152:155], v[220:223], v[82:85]
	v_mfma_f32_16x16x32_bf16 v[74:77], v[160:163], v[220:223], v[74:77]
	s_setprio 0
	s_setprio 1
	v_mfma_f32_16x16x32_bf16 v[118:121], v[176:179], v[192:195], v[118:121]
	v_mfma_f32_16x16x32_bf16 v[110:113], v[184:187], v[192:195], v[110:113]
	v_mfma_f32_16x16x32_bf16 v[102:105], v[176:179], v[200:203], v[102:105]
	v_mfma_f32_16x16x32_bf16 v[94:97], v[184:187], v[200:203], v[94:97]
	v_mfma_f32_16x16x32_bf16 v[86:89], v[176:179], v[208:211], v[86:89]
	v_mfma_f32_16x16x32_bf16 v[78:81], v[184:187], v[208:211], v[78:81]
	v_mfma_f32_16x16x32_bf16 v[70:73], v[176:179], v[216:219], v[70:73]
	v_mfma_f32_16x16x32_bf16 v[66:69], v[184:187], v[216:219], v[66:69]
	v_mfma_f32_16x16x32_bf16 v[118:121], v[180:183], v[196:199], v[118:121]
	v_mfma_f32_16x16x32_bf16 v[110:113], v[188:191], v[196:199], v[110:113]
	v_mfma_f32_16x16x32_bf16 v[102:105], v[180:183], v[204:207], v[102:105]
	v_mfma_f32_16x16x32_bf16 v[94:97], v[188:191], v[204:207], v[94:97]
	v_mfma_f32_16x16x32_bf16 v[86:89], v[180:183], v[212:215], v[86:89]
	v_mfma_f32_16x16x32_bf16 v[78:81], v[188:191], v[212:215], v[78:81]
	v_mfma_f32_16x16x32_bf16 v[70:73], v[180:183], v[220:223], v[70:73]
	v_mfma_f32_16x16x32_bf16 v[66:69], v[188:191], v[220:223], v[66:69]
	s_setprio 0
	s_barrier
; #define PG8_STAGE_A(b, h, ptr, NX) do { if constexpr (Sched::GATHER) { unsigned gs_[2]; gs_[0] = ((NX) && last_) ? gN[h][0] : gA[h][0]; gs_[1] = ((NX) && last_) ? gN[h][1] : gA[h][1]; PG8_STAGE(PG8_SA(b, h), ptr, gs_); } \
;         else PG8_STAGE(PG8_SA(b, h), (ptr) + ((h) ? hstep : (size_t)0), voffA); } while (0)
; #define PG8_STAGE(bufoff, gbase, voff) do { _Pragma("unroll") for (int _i = 0; _i < 2; ++_i) \
;         __builtin_amdgcn_global_load_lds((const unsigned*)((const char*)(gbase) + (voff)[_i]), (PG8_LAS unsigned*)(lds + (bufoff) + ldsw + _i * 8192), 16, 0, 0); } while (0)
; #define PG8_LDA(dst, b, h) do { _Pragma("unroll") for (int m = 0; m < 4; ++m) _Pragma("unroll") for (int k = 0; k < 2; ++k) dst[m][k] = *(const PG8_LAS bf16x8*)(lds + PG8_SA(b, h) + aoff + m * 2048 + k * 1024); } while (0)
; #define PG8_LDB(dst, b, h) do { _Pragma("unroll") for (int n = 0; n < 2; ++n) _Pragma("unroll") for (int k = 0; k < 2; ++k) dst[n][k] = *(const PG8_LAS bf16x8*)(lds + PG8_SB(b, h) + boff + n * 2048 + k * 1024); } while (0)
; #define PG8_MMA(ai, bj, At, Bt) do { __builtin_amdgcn_s_setprio(1); _Pragma("unroll") for (int m = 0; m < 4; ++m) _Pragma("unroll") for (int n = 0; n < 2; ++n) _Pragma("unroll") for (int k = 0; k < 2; ++k) \
;         acc[ai][bj][m][n] = __builtin_amdgcn_mfma_f32_16x16x32_bf16(Bt[n][k], At[m][k], acc[ai][bj][m][n], 0, 0, 0); __builtin_amdgcn_s_setprio(0); } while (0)
; #define PG8_WAIT_V(n) asm volatile("s_waitcnt vmcnt(" #n ")" ::: "memory")
; #define PG8_WAIT_L(n) asm volatile("s_waitcnt lgkmcnt(" #n ")" ::: "memory")
; #define PG8_BAR __builtin_amdgcn_s_barrier()
; #define PG8_SCHED __builtin_amdgcn_sched_barrier(0)
; template <class Epi, class Sched, bool ALIGN_EPI = false, bool SP2 = false>
; __device__ __forceinline__ void gemm_phase(PG8_LAS unsigned char* lds, const Gemm g, const Sched& S, const Epi& E, const bool skip_epi = false) {
;     ...
;             PG8_LDB(B0, 0, 0); PG8_LDB(B1, 0, 1); PG8_SCHED; PG8_LDA(At, 0, 0); PG8_STAGE_A(1, 1, a1, false);
;             PG8_WAIT_V(8); PG8_WAIT_L(0); PG8_BAR; PG8_MMA(0, 0, At, B0); PG8_MMA(0, 1, At, B1); PG8_BAR; PG8_SCHED;
;     ...
;             PG8_LDA(At, 1, 1); PG8_STAGE(PG8_SB(1, 0), b3, voffB); PG8_STAGE(PG8_SB(1, 1), b3 + hstep, voffB); PG8_STAGE_A(1, 0, a3, true);
;             PG8_WAIT_V(8); PG8_WAIT_L(0); PG8_BAR; PG8_MMA(1, 0, At, B0); PG8_MMA(1, 1, At, B1); PG8_BAR; PG8_SCHED;
	s_add_i32 s28, s61, s2
	v_lshl_add_u64 v[164:165], v[164:165], 0, s[10:11]
	s_mov_b32 m0, s28
	ds_read_b128 v[192:195], v172 offset:49152
	ds_read_b128 v[196:199], v172 offset:50176
	ds_read_b128 v[200:203], v172 offset:51200
	ds_read_b128 v[204:207], v172 offset:52224
	ds_read_b128 v[208:211], v172 offset:53248
	ds_read_b128 v[212:215], v172 offset:54272
	ds_read_b128 v[216:219], v172 offset:55296
	ds_read_b128 v[220:223], v172 offset:56320
	global_load_lds_dwordx4 v[164:165], off
	s_add_i32 m0, s28, 0x2000
	s_add_u32 s26, s26, 0x40080
	v_lshl_add_u64 v[164:165], v[224:225], 0, s[10:11]
	s_addc_u32 s27, s27, 0
	s_add_i32 s28, s62, s2
	global_load_lds_dwordx4 v[164:165], off
	v_lshl_add_u64 v[164:165], s[26:27], 0, v[134:135]
	s_mov_b32 m0, s28
	s_nop 0
	global_load_lds_dwordx4 v[164:165], off
	v_lshl_add_u64 v[164:165], s[26:27], 0, v[130:131]
	s_add_i32 m0, s28, 0x2000
	s_nop 0
	global_load_lds_dwordx4 v[164:165], off
	v_lshl_add_u64 v[164:165], v[226:227], 0, s[10:11]
	s_mov_b32 m0, s37
	s_nop 0
	global_load_lds_dwordx4 v[164:165], off
	v_lshl_add_u64 v[164:165], v[230:231], 0, s[10:11]
	s_mov_b32 m0, s38
	s_nop 0
	global_load_lds_dwordx4 v[164:165], off
	s_waitcnt vmcnt(8)
	s_waitcnt lgkmcnt(0)
	s_barrier
	s_setprio 1
	s_waitcnt lgkmcnt(0)
	v_mfma_f32_16x16x32_bf16 v[62:65], v[148:151], v[192:195], v[62:65]
	v_mfma_f32_16x16x32_bf16 v[58:61], v[156:159], v[192:195], v[58:61]
	v_mfma_f32_16x16x32_bf16 v[50:53], v[148:151], v[200:203], v[50:53]
	v_mfma_f32_16x16x32_bf16 v[42:45], v[156:159], v[200:203], v[42:45]
	v_mfma_f32_16x16x32_bf16 v[34:37], v[148:151], v[208:211], v[34:37]
	v_mfma_f32_16x16x32_bf16 v[26:29], v[156:159], v[208:211], v[26:29]
	v_mfma_f32_16x16x32_bf16 v[18:21], v[148:151], v[216:219], v[18:21]
	v_mfma_f32_16x16x32_bf16 v[10:13], v[156:159], v[216:219], v[10:13]
	v_mfma_f32_16x16x32_bf16 v[62:65], v[152:155], v[196:199], v[62:65]
	v_mfma_f32_16x16x32_bf16 v[58:61], v[160:163], v[196:199], v[58:61]
	v_mfma_f32_16x16x32_bf16 v[50:53], v[152:155], v[204:207], v[50:53]
	v_mfma_f32_16x16x32_bf16 v[42:45], v[160:163], v[204:207], v[42:45]
	v_mfma_f32_16x16x32_bf16 v[34:37], v[152:155], v[212:215], v[34:37]
	v_mfma_f32_16x16x32_bf16 v[26:29], v[160:163], v[212:215], v[26:29]
	v_mfma_f32_16x16x32_bf16 v[18:21], v[152:155], v[220:223], v[18:21]
	v_mfma_f32_16x16x32_bf16 v[10:13], v[160:163], v[220:223], v[10:13]
	s_setprio 0
	s_setprio 1
	v_mfma_f32_16x16x32_bf16 v[54:57], v[176:179], v[192:195], v[54:57]
	v_mfma_f32_16x16x32_bf16 v[46:49], v[184:187], v[192:195], v[46:49]
	v_mfma_f32_16x16x32_bf16 v[38:41], v[176:179], v[200:203], v[38:41]
	v_mfma_f32_16x16x32_bf16 v[30:33], v[184:187], v[200:203], v[30:33]
	v_mfma_f32_16x16x32_bf16 v[22:25], v[176:179], v[208:211], v[22:25]
	v_mfma_f32_16x16x32_bf16 v[14:17], v[184:187], v[208:211], v[14:17]
	v_mfma_f32_16x16x32_bf16 v[6:9], v[176:179], v[216:219], v[6:9]
	v_mfma_f32_16x16x32_bf16 v[2:5], v[184:187], v[216:219], v[2:5]
	v_mfma_f32_16x16x32_bf16 v[54:57], v[180:183], v[196:199], v[54:57]
	v_mfma_f32_16x16x32_bf16 v[46:49], v[188:191], v[196:199], v[46:49]
	v_mfma_f32_16x16x32_bf16 v[38:41], v[180:183], v[204:207], v[38:41]
	v_mfma_f32_16x16x32_bf16 v[30:33], v[188:191], v[204:207], v[30:33]
	v_mfma_f32_16x16x32_bf16 v[22:25], v[180:183], v[212:215], v[22:25]
	v_mfma_f32_16x16x32_bf16 v[14:17], v[188:191], v[212:215], v[14:17]
	v_mfma_f32_16x16x32_bf16 v[6:9], v[180:183], v[220:223], v[6:9]
	v_mfma_f32_16x16x32_bf16 v[2:5], v[188:191], v[220:223], v[2:5]
	s_setprio 0
	s_barrier
	s_add_i32 s60, s60, 2
	s_add_u32 s24, s24, 0x100
	s_addc_u32 s25, s25, 0
	s_add_u32 s58, s58, 0x100
	s_addc_u32 s59, s59, 0
	s_cmp_gt_u32 s60, 13
.LBB0_253:
	ds_read_b128 v[148:151], v170
	ds_read_b128 v[152:155], v170 offset:1024
	ds_read_b128 v[156:159], v170 offset:2048
	ds_read_b128 v[160:163], v170 offset:3072
	ds_read_b128 v[176:179], v171
	ds_read_b128 v[180:183], v171 offset:1024
	ds_read_b128 v[184:187], v171 offset:2048
	ds_read_b128 v[188:191], v171 offset:3072
	s_add_u32 s26, s24, 0xfffc0080
	s_addc_u32 s27, s25, -1
	s_cmp_eq_u32 s60, 12
	s_cselect_b32 s29, s17, s27
	s_cselect_b32 s28, s56, s26
	s_cselect_b32 s27, s15, s59
	s_cselect_b32 s26, s57, s58
	v_lshl_add_u64 v[164:165], s[24:25], 0, v[140:141]
	s_add_i32 m0, s23, 0xc000
	ds_read_b128 v[192:195], v172
	ds_read_b128 v[196:199], v172 offset:1024
	ds_read_b128 v[200:203], v172 offset:2048
	ds_read_b128 v[204:207], v172 offset:3072
	ds_read_b128 v[208:211], v172 offset:4096
	ds_read_b128 v[212:215], v172 offset:5120
	ds_read_b128 v[216:219], v172 offset:6144
	ds_read_b128 v[220:223], v172 offset:7168
	global_load_lds_dwordx4 v[164:165], off
	v_lshl_add_u64 v[164:165], s[24:25], 0, v[142:143]
	s_add_i32 m0, s23, 0xe000
	s_nop 0
	global_load_lds_dwordx4 v[164:165], off
	s_waitcnt vmcnt(8)
	s_waitcnt lgkmcnt(0)
	s_barrier
; #define PG8_STAGE_A(b, h, ptr, NX) do { if constexpr (Sched::GATHER) { unsigned gs_[2]; gs_[0] = ((NX) && last_) ? gN[h][0] : gA[h][0]; gs_[1] = ((NX) && last_) ? gN[h][1] : gA[h][1]; PG8_STAGE(PG8_SA(b, h), ptr, gs_); } \
;         else PG8_STAGE(PG8_SA(b, h), (ptr) + ((h) ? hstep : (size_t)0), voffA); } while (0)
; #define PG8_STAGE(bufoff, gbase, voff) do { _Pragma("unroll") for (int _i = 0; _i < 2; ++_i) \
;         __builtin_amdgcn_global_load_lds((const unsigned*)((const char*)(gbase) + (voff)[_i]), (PG8_LAS unsigned*)(lds + (bufoff) + ldsw + _i * 8192), 16, 0, 0); } while (0)
; #define PG8_LDA(dst, b, h) do { _Pragma("unroll") for (int m = 0; m < 4; ++m) _Pragma("unroll") for (int k = 0; k < 2; ++k) dst[m][k] = *(const PG8_LAS bf16x8*)(lds + PG8_SA(b, h) + aoff + m * 2048 + k * 1024); } while (0)
; #define PG8_LDB(dst, b, h) do { _Pragma("unroll") for (int n = 0; n < 2; ++n) _Pragma("unroll") for (int k = 0; k < 2; ++k) dst[n][k] = *(const PG8_LAS bf16x8*)(lds + PG8_SB(b, h) + boff + n * 2048 + k * 1024); } while (0)
; #define PG8_MMA(ai, bj, At, Bt) do { __builtin_amdgcn_s_setprio(1); _Pragma("unroll") for (int m = 0; m < 4; ++m) _Pragma("unroll") for (int n = 0; n < 2; ++n) _Pragma("unroll") for (int k = 0; k < 2; ++k) \
;         acc[ai][bj][m][n] = __builtin_amdgcn_mfma_f32_16x16x32_bf16(Bt[n][k], At[m][k], acc[ai][bj][m][n], 0, 0, 0); __builtin_amdgcn_s_setprio(0); } while (0)
; template <class Epi, class Sched, bool ALIGN_EPI = false, bool SP2 = false>
; __device__ __forceinline__ void gemm_phase(PG8_LAS unsigned char* lds, const Gemm g, const Sched& S, const Epi& E, const bool skip_epi = false) {
;     ...
;             PG8_LDB(B0, 0, 0); PG8_LDB(B1, 0, 1); PG8_SCHED; PG8_LDA(At, 0, 0); PG8_STAGE_A(1, 1, a1, false);
;             PG8_WAIT_V(8); PG8_WAIT_L(0); PG8_BAR; PG8_MMA(0, 0, At, B0); PG8_MMA(0, 1, At, B1); PG8_BAR; PG8_SCHED;
;             PG8_LDA(At, 0, 1); PG8_STAGE(PG8_SB(0, 0), b2, voffB); PG8_STAGE(PG8_SB(0, 1), b2 + hstep, voffB); PG8_STAGE_A(0, 0, a2, true);
;             PG8_WAIT_V(8); PG8_WAIT_L(0); PG8_BAR; PG8_MMA(1, 0, At, B0); PG8_MMA(1, 1, At, B1); PG8_BAR; PG8_SCHED;
;             PG8_LDB(B0, 1, 0); PG8_LDB(B1, 1, 1); PG8_SCHED; PG8_LDA(At, 1, 0); PG8_STAGE_A(0, 1, a2, true);
;             PG8_WAIT_V(8); PG8_WAIT_L(0); PG8_BAR; PG8_MMA(0, 0, At, B0); PG8_MMA(0, 1, At, B1); PG8_BAR; PG8_SCHED;
	s_setprio 1
	s_waitcnt lgkmcnt(0)
	v_mfma_f32_16x16x32_bf16 v[126:129], v[148:151], v[192:195], v[126:129]
	v_mfma_f32_16x16x32_bf16 v[122:125], v[156:159], v[192:195], v[122:125]
	v_mfma_f32_16x16x32_bf16 v[114:117], v[148:151], v[200:203], v[114:117]
	v_mfma_f32_16x16x32_bf16 v[106:109], v[156:159], v[200:203], v[106:109]
	v_mfma_f32_16x16x32_bf16 v[98:101], v[148:151], v[208:211], v[98:101]
	v_mfma_f32_16x16x32_bf16 v[90:93], v[156:159], v[208:211], v[90:93]
	v_mfma_f32_16x16x32_bf16 v[82:85], v[148:151], v[216:219], v[82:85]
	v_mfma_f32_16x16x32_bf16 v[74:77], v[156:159], v[216:219], v[74:77]
	v_mfma_f32_16x16x32_bf16 v[126:129], v[152:155], v[196:199], v[126:129]
	v_mfma_f32_16x16x32_bf16 v[122:125], v[160:163], v[196:199], v[122:125]
	v_mfma_f32_16x16x32_bf16 v[114:117], v[152:155], v[204:207], v[114:117]
	v_mfma_f32_16x16x32_bf16 v[106:109], v[160:163], v[204:207], v[106:109]
	v_mfma_f32_16x16x32_bf16 v[98:101], v[152:155], v[212:215], v[98:101]
	v_mfma_f32_16x16x32_bf16 v[90:93], v[160:163], v[212:215], v[90:93]
	v_mfma_f32_16x16x32_bf16 v[82:85], v[152:155], v[220:223], v[82:85]
	v_mfma_f32_16x16x32_bf16 v[74:77], v[160:163], v[220:223], v[74:77]
	s_setprio 0
	s_setprio 1
	v_mfma_f32_16x16x32_bf16 v[118:121], v[176:179], v[192:195], v[118:121]
	v_mfma_f32_16x16x32_bf16 v[110:113], v[184:187], v[192:195], v[110:113]
	v_mfma_f32_16x16x32_bf16 v[102:105], v[176:179], v[200:203], v[102:105]
	v_mfma_f32_16x16x32_bf16 v[94:97], v[184:187], v[200:203], v[94:97]
	v_mfma_f32_16x16x32_bf16 v[86:89], v[176:179], v[208:211], v[86:89]
	v_mfma_f32_16x16x32_bf16 v[78:81], v[184:187], v[208:211], v[78:81]
	v_mfma_f32_16x16x32_bf16 v[70:73], v[176:179], v[216:219], v[70:73]
	v_mfma_f32_16x16x32_bf16 v[66:69], v[184:187], v[216:219], v[66:69]
	v_mfma_f32_16x16x32_bf16 v[118:121], v[180:183], v[196:199], v[118:121]
	v_mfma_f32_16x16x32_bf16 v[110:113], v[188:191], v[196:199], v[110:113]
	v_mfma_f32_16x16x32_bf16 v[102:105], v[180:183], v[204:207], v[102:105]
	v_mfma_f32_16x16x32_bf16 v[94:97], v[188:191], v[204:207], v[94:97]
	v_mfma_f32_16x16x32_bf16 v[86:89], v[180:183], v[212:215], v[86:89]
	v_mfma_f32_16x16x32_bf16 v[78:81], v[188:191], v[212:215], v[78:81]
	v_mfma_f32_16x16x32_bf16 v[70:73], v[180:183], v[220:223], v[70:73]
	v_mfma_f32_16x16x32_bf16 v[66:69], v[188:191], v[220:223], v[66:69]
	s_setprio 0
	s_barrier
	s_add_i32 s61, s46, s2
	v_lshl_add_u64 v[164:165], s[26:27], 0, v[134:135]
	s_mov_b32 m0, s61
	ds_read_b128 v[192:195], v172 offset:16384
	ds_read_b128 v[196:199], v172 offset:17408
	ds_read_b128 v[200:203], v172 offset:18432
	ds_read_b128 v[204:207], v172 offset:19456
	ds_read_b128 v[208:211], v172 offset:20480
	ds_read_b128 v[212:215], v172 offset:21504
	ds_read_b128 v[216:219], v172 offset:22528
	ds_read_b128 v[220:223], v172 offset:23552
	global_load_lds_dwordx4 v[164:165], off
	s_add_i32 m0, s61, 0x2000
	s_add_u32 s62, s26, 0x40000
	v_lshl_add_u64 v[224:225], s[26:27], 0, v[130:131]
	s_addc_u32 s63, s27, 0
	s_add_i32 s61, s47, s2
	global_load_lds_dwordx4 v[224:225], off
	v_lshl_add_u64 v[226:227], s[62:63], 0, v[134:135]
	s_mov_b32 m0, s61
	v_lshl_add_u64 v[230:231], s[28:29], 0, v[132:133]
	global_load_lds_dwordx4 v[226:227], off
	v_lshl_add_u64 v[226:227], s[62:63], 0, v[130:131]
	s_add_i32 m0, s61, 0x2000
	s_nop 0
	global_load_lds_dwordx4 v[226:227], off
	v_lshl_add_u64 v[226:227], s[28:29], 0, v[136:137]
	s_mov_b32 m0, s23
	s_nop 0
	global_load_lds_dwordx4 v[226:227], off
	s_mov_b32 m0, s31
	s_nop 0
	global_load_lds_dwordx4 v[230:231], off
	s_waitcnt vmcnt(8)
	s_waitcnt lgkmcnt(0)
	s_barrier
	s_setprio 1
	s_waitcnt lgkmcnt(0)
	v_mfma_f32_16x16x32_bf16 v[62:65], v[148:151], v[192:195], v[62:65]
	v_mfma_f32_16x16x32_bf16 v[58:61], v[156:159], v[192:195], v[58:61]
	v_mfma_f32_16x16x32_bf16 v[50:53], v[148:151], v[200:203], v[50:53]
	v_mfma_f32_16x16x32_bf16 v[42:45], v[156:159], v[200:203], v[42:45]
	v_mfma_f32_16x16x32_bf16 v[34:37], v[148:151], v[208:211], v[34:37]
	v_mfma_f32_16x16x32_bf16 v[26:29], v[156:159], v[208:211], v[26:29]
	v_mfma_f32_16x16x32_bf16 v[18:21], v[148:151], v[216:219], v[18:21]
	v_mfma_f32_16x16x32_bf16 v[10:13], v[156:159], v[216:219], v[10:13]
	v_mfma_f32_16x16x32_bf16 v[62:65], v[152:155], v[196:199], v[62:65]
	v_mfma_f32_16x16x32_bf16 v[58:61], v[160:163], v[196:199], v[58:61]
	v_mfma_f32_16x16x32_bf16 v[50:53], v[152:155], v[204:207], v[50:53]
	v_mfma_f32_16x16x32_bf16 v[42:45], v[160:163], v[204:207], v[42:45]
	v_mfma_f32_16x16x32_bf16 v[34:37], v[152:155], v[212:215], v[34:37]
	v_mfma_f32_16x16x32_bf16 v[26:29], v[160:163], v[212:215], v[26:29]
	v_mfma_f32_16x16x32_bf16 v[18:21], v[152:155], v[220:223], v[18:21]
	v_mfma_f32_16x16x32_bf16 v[10:13], v[160:163], v[220:223], v[10:13]
	s_setprio 0
	s_setprio 1
	v_mfma_f32_16x16x32_bf16 v[54:57], v[176:179], v[192:195], v[54:57]
	v_mfma_f32_16x16x32_bf16 v[46:49], v[184:187], v[192:195], v[46:49]
	v_mfma_f32_16x16x32_bf16 v[38:41], v[176:179], v[200:203], v[38:41]
	v_mfma_f32_16x16x32_bf16 v[30:33], v[184:187], v[200:203], v[30:33]
	v_mfma_f32_16x16x32_bf16 v[22:25], v[176:179], v[208:211], v[22:25]
	v_mfma_f32_16x16x32_bf16 v[14:17], v[184:187], v[208:211], v[14:17]
	v_mfma_f32_16x16x32_bf16 v[6:9], v[176:179], v[216:219], v[6:9]
	v_mfma_f32_16x16x32_bf16 v[2:5], v[184:187], v[216:219], v[2:5]
	v_mfma_f32_16x16x32_bf16 v[54:57], v[180:183], v[196:199], v[54:57]
	v_mfma_f32_16x16x32_bf16 v[46:49], v[188:191], v[196:199], v[46:49]
	v_mfma_f32_16x16x32_bf16 v[38:41], v[180:183], v[204:207], v[38:41]
	v_mfma_f32_16x16x32_bf16 v[30:33], v[188:191], v[204:207], v[30:33]
	v_mfma_f32_16x16x32_bf16 v[22:25], v[180:183], v[212:215], v[22:25]
	v_mfma_f32_16x16x32_bf16 v[14:17], v[188:191], v[212:215], v[14:17]
	v_mfma_f32_16x16x32_bf16 v[6:9], v[180:183], v[220:223], v[6:9]
	v_mfma_f32_16x16x32_bf16 v[2:5], v[188:191], v[220:223], v[2:5]
	s_setprio 0
	s_barrier
; #define PG8_STAGE_A(b, h, ptr, NX) do { if constexpr (Sched::GATHER) { unsigned gs_[2]; gs_[0] = ((NX) && last_) ? gN[h][0] : gA[h][0]; gs_[1] = ((NX) && last_) ? gN[h][1] : gA[h][1]; PG8_STAGE(PG8_SA(b, h), ptr, gs_); } \
;         else PG8_STAGE(PG8_SA(b, h), (ptr) + ((h) ? hstep : (size_t)0), voffA); } while (0)
; #define PG8_STAGE(bufoff, gbase, voff) do { _Pragma("unroll") for (int _i = 0; _i < 2; ++_i) \
;         __builtin_amdgcn_global_load_lds((const unsigned*)((const char*)(gbase) + (voff)[_i]), (PG8_LAS unsigned*)(lds + (bufoff) + ldsw + _i * 8192), 16, 0, 0); } while (0)
; #define PG8_LDA(dst, b, h) do { _Pragma("unroll") for (int m = 0; m < 4; ++m) _Pragma("unroll") for (int k = 0; k < 2; ++k) dst[m][k] = *(const PG8_LAS bf16x8*)(lds + PG8_SA(b, h) + aoff + m * 2048 + k * 1024); } while (0)
; #define PG8_LDB(dst, b, h) do { _Pragma("unroll") for (int n = 0; n < 2; ++n) _Pragma("unroll") for (int k = 0; k < 2; ++k) dst[n][k] = *(const PG8_LAS bf16x8*)(lds + PG8_SB(b, h) + boff + n * 2048 + k * 1024); } while (0)
; #define PG8_MMA(ai, bj, At, Bt) do { __builtin_amdgcn_s_setprio(1); _Pragma("unroll") for (int m = 0; m < 4; ++m) _Pragma("unroll") for (int n = 0; n < 2; ++n) _Pragma("unroll") for (int k = 0; k < 2; ++k) \
;         acc[ai][bj][m][n] = __builtin_amdgcn_mfma_f32_16x16x32_bf16(Bt[n][k], At[m][k], acc[ai][bj][m][n], 0, 0, 0); __builtin_amdgcn_s_setprio(0); } while (0)
; #define PG8_WAIT_V(n) asm volatile("s_waitcnt vmcnt(" #n ")" ::: "memory")
; #define PG8_WAIT_L(n) asm volatile("s_waitcnt lgkmcnt(" #n ")" ::: "memory")
; #define PG8_BAR __builtin_amdgcn_s_barrier()
; #define PG8_SCHED __builtin_amdgcn_sched_barrier(0)
; template <class Epi, class Sched, bool ALIGN_EPI = false, bool SP2 = false>
; __device__ __forceinline__ void gemm_phase(PG8_LAS unsigned char* lds, const Gemm g, const Sched& S, const Epi& E, const bool skip_epi = false) {
;     ...
;             PG8_LDB(B0, 1, 0); PG8_LDB(B1, 1, 1); PG8_SCHED; PG8_LDA(At, 1, 0); PG8_STAGE_A(0, 1, a2, true);
;             PG8_WAIT_V(8); PG8_WAIT_L(0); PG8_BAR; PG8_MMA(0, 0, At, B0); PG8_MMA(0, 1, At, B1); PG8_BAR; PG8_SCHED;
;             PG8_LDA(At, 1, 1); PG8_STAGE(PG8_SB(1, 0), b3, voffB); PG8_STAGE(PG8_SB(1, 1), b3 + hstep, voffB); PG8_STAGE_A(1, 0, a3, true);
;             PG8_WAIT_V(8); PG8_WAIT_L(0); PG8_BAR; PG8_MMA(1, 0, At, B0); PG8_MMA(1, 1, At, B1); PG8_BAR; PG8_SCHED;
	s_add_i32 s61, 0, 0x18000
	s_add_i32 s62, 0, 0x1c000
	v_add_u32_e32 v160, s61, v1
	v_add_u32_e32 v188, s62, v1
	ds_read_b128 v[148:151], v160
	ds_read_b128 v[152:155], v160 offset:1024
	ds_read_b128 v[156:159], v160 offset:2048
	ds_read_b128 v[160:163], v160 offset:3072
	ds_read_b128 v[176:179], v188
	ds_read_b128 v[180:183], v188 offset:1024
	ds_read_b128 v[184:187], v188 offset:2048
	ds_read_b128 v[188:191], v188 offset:3072
	s_add_u32 s28, s28, 0x40000
	s_addc_u32 s29, s29, 0
	s_mov_b32 m0, s34
	v_lshl_add_u64 v[232:233], s[28:29], 0, v[136:137]
	ds_read_b128 v[192:195], v172 offset:32768
	ds_read_b128 v[196:199], v172 offset:33792
	ds_read_b128 v[200:203], v172 offset:34816
	ds_read_b128 v[204:207], v172 offset:35840
	ds_read_b128 v[208:211], v172 offset:36864
	ds_read_b128 v[212:215], v172 offset:37888
	ds_read_b128 v[216:219], v172 offset:38912
	ds_read_b128 v[220:223], v172 offset:39936
	global_load_lds_dwordx4 v[232:233], off
	v_lshl_add_u64 v[232:233], s[28:29], 0, v[132:133]
	s_mov_b32 m0, s35
	s_nop 0
	global_load_lds_dwordx4 v[232:233], off
	s_waitcnt vmcnt(8)
	s_waitcnt lgkmcnt(0)
	s_barrier
	s_setprio 1
	s_waitcnt lgkmcnt(0)
	v_mfma_f32_16x16x32_bf16 v[126:129], v[148:151], v[192:195], v[126:129]
	v_mfma_f32_16x16x32_bf16 v[122:125], v[156:159], v[192:195], v[122:125]
	v_mfma_f32_16x16x32_bf16 v[114:117], v[148:151], v[200:203], v[114:117]
	v_mfma_f32_16x16x32_bf16 v[106:109], v[156:159], v[200:203], v[106:109]
	v_mfma_f32_16x16x32_bf16 v[98:101], v[148:151], v[208:211], v[98:101]
	v_mfma_f32_16x16x32_bf16 v[90:93], v[156:159], v[208:211], v[90:93]
	v_mfma_f32_16x16x32_bf16 v[82:85], v[148:151], v[216:219], v[82:85]
	v_mfma_f32_16x16x32_bf16 v[74:77], v[156:159], v[216:219], v[74:77]
	v_mfma_f32_16x16x32_bf16 v[126:129], v[152:155], v[196:199], v[126:129]
	v_mfma_f32_16x16x32_bf16 v[122:125], v[160:163], v[196:199], v[122:125]
	v_mfma_f32_16x16x32_bf16 v[114:117], v[152:155], v[204:207], v[114:117]
	v_mfma_f32_16x16x32_bf16 v[106:109], v[160:163], v[204:207], v[106:109]
	v_mfma_f32_16x16x32_bf16 v[98:101], v[152:155], v[212:215], v[98:101]
	v_mfma_f32_16x16x32_bf16 v[90:93], v[160:163], v[212:215], v[90:93]
	v_mfma_f32_16x16x32_bf16 v[82:85], v[152:155], v[220:223], v[82:85]
	v_mfma_f32_16x16x32_bf16 v[74:77], v[160:163], v[220:223], v[74:77]
	s_setprio 0
	s_setprio 1
	v_mfma_f32_16x16x32_bf16 v[118:121], v[176:179], v[192:195], v[118:121]
	v_mfma_f32_16x16x32_bf16 v[110:113], v[184:187], v[192:195], v[110:113]
	v_mfma_f32_16x16x32_bf16 v[102:105], v[176:179], v[200:203], v[102:105]
	v_mfma_f32_16x16x32_bf16 v[94:97], v[184:187], v[200:203], v[94:97]
	v_mfma_f32_16x16x32_bf16 v[86:89], v[176:179], v[208:211], v[86:89]
	v_mfma_f32_16x16x32_bf16 v[78:81], v[184:187], v[208:211], v[78:81]
	v_mfma_f32_16x16x32_bf16 v[70:73], v[176:179], v[216:219], v[70:73]
	v_mfma_f32_16x16x32_bf16 v[66:69], v[184:187], v[216:219], v[66:69]
	v_mfma_f32_16x16x32_bf16 v[118:121], v[180:183], v[196:199], v[118:121]
	v_mfma_f32_16x16x32_bf16 v[110:113], v[188:191], v[196:199], v[110:113]
	v_mfma_f32_16x16x32_bf16 v[102:105], v[180:183], v[204:207], v[102:105]
	v_mfma_f32_16x16x32_bf16 v[94:97], v[188:191], v[204:207], v[94:97]
	v_mfma_f32_16x16x32_bf16 v[86:89], v[180:183], v[212:215], v[86:89]
	v_mfma_f32_16x16x32_bf16 v[78:81], v[188:191], v[212:215], v[78:81]
	v_mfma_f32_16x16x32_bf16 v[70:73], v[180:183], v[220:223], v[70:73]
	v_mfma_f32_16x16x32_bf16 v[66:69], v[188:191], v[220:223], v[66:69]
	s_setprio 0
	s_barrier
	s_add_i32 s28, s61, s2
	v_lshl_add_u64 v[164:165], v[164:165], 0, s[10:11]
	s_mov_b32 m0, s28
	ds_read_b128 v[192:195], v172 offset:49152
	ds_read_b128 v[196:199], v172 offset:50176
	ds_read_b128 v[200:203], v172 offset:51200
	ds_read_b128 v[204:207], v172 offset:52224
	ds_read_b128 v[208:211], v172 offset:53248
	ds_read_b128 v[212:215], v172 offset:54272
	ds_read_b128 v[216:219], v172 offset:55296
	ds_read_b128 v[220:223], v172 offset:56320
	global_load_lds_dwordx4 v[164:165], off
	s_add_i32 m0, s28, 0x2000
	s_add_u32 s26, s26, 0x40080
	v_lshl_add_u64 v[164:165], v[224:225], 0, s[10:11]
	s_addc_u32 s27, s27, 0
	s_add_i32 s28, s62, s2
	global_load_lds_dwordx4 v[164:165], off
	v_lshl_add_u64 v[164:165], s[26:27], 0, v[134:135]
	s_mov_b32 m0, s28
	s_nop 0
	global_load_lds_dwordx4 v[164:165], off
	v_lshl_add_u64 v[164:165], s[26:27], 0, v[130:131]
	s_add_i32 m0, s28, 0x2000
	s_nop 0
	global_load_lds_dwordx4 v[164:165], off
	v_lshl_add_u64 v[164:165], v[226:227], 0, s[10:11]
	s_mov_b32 m0, s37
	s_nop 0
	global_load_lds_dwordx4 v[164:165], off
	v_lshl_add_u64 v[164:165], v[230:231], 0, s[10:11]
	s_mov_b32 m0, s38
	s_nop 0
	global_load_lds_dwordx4 v[164:165], off
	s_waitcnt vmcnt(8)
	s_waitcnt lgkmcnt(0)
	s_barrier
; #define PG8_MMA(ai, bj, At, Bt) do { __builtin_amdgcn_s_setprio(1); _Pragma("unroll") for (int m = 0; m < 4; ++m) _Pragma("unroll") for (int n = 0; n < 2; ++n) _Pragma("unroll") for (int k = 0; k < 2; ++k) \
;         acc[ai][bj][m][n] = __builtin_amdgcn_mfma_f32_16x16x32_bf16(Bt[n][k], At[m][k], acc[ai][bj][m][n], 0, 0, 0); __builtin_amdgcn_s_setprio(0); } while (0)
; #define PG8_WAIT_V(n) asm volatile("s_waitcnt vmcnt(" #n ")" ::: "memory")
; #define PG8_WAIT_L(n) asm volatile("s_waitcnt lgkmcnt(" #n ")" ::: "memory")
; #define PG8_BAR __builtin_amdgcn_s_barrier()
; #define PG8_SCHED __builtin_amdgcn_sched_barrier(0)
; __device__ __forceinline__ void rstd8(const float* SS, int rowb, int lane, float (&rs)[2][4]) {
;     ...
;         for (int m = 0; m < 4; ++m) p[ai][m] = *(const f32x4*)(SS + (size_t)(rowb + HALF * ai + 16 * m + (lane >> 2)) * 16 + 4 * (lane & 3));
;     asm volatile("" : "+v"(p[0][0]), "+v"(p[0][1]), "+v"(p[0][2]), "+v"(p[0][3]), "+v"(p[1][0]), "+v"(p[1][1]), "+v"(p[1][2]), "+v"(p[1][3]));
; #pragma unroll
;     for (int ai = 0; ai < 2; ++ai)
; #pragma unroll
;         for (int m = 0; m < 4; ++m) { float s = (p[ai][m][0] + p[ai][m][1]) + (p[ai][m][2] + p[ai][m][3]); s += __shfl_xor(s, 1); s += __shfl_xor(s, 2);
;             const float r = __builtin_amdgcn_rsqf(s * (1.0f / 1024.0f) + RMS_EPS);
;             rs[ai][m] = __builtin_bit_cast(float, __builtin_amdgcn_ds_bpermute((lane & 15) << 4, __builtin_bit_cast(int, r))); }
;     __device__ __forceinline__ void operator()(const f32x4 (&acc)[2][2][4][2], const Unit& u, int wr, int wc, int fr, int fq) const {
;         const int row0 = u.pm * BM + wr * 64 + fr, col0 = u.pn * BM + wc * 32 + 8 * fq;
;         const float sc = (u.pn == 0) ? qs : ((u.pn == 3) ? 0.125f : 1.0f);
;         const int lane = fr + 16 * fq, qs4 = QSRC_ST(lane); const int rowS = u.pm * BM + wr * 64 + (lane >> 2), colS = u.pn * BM + wc * 32 + 8 * (lane & 3);
;         float rs8[2][4]; rstd8(SS, u.pm * BM + wr * 64, lane, rs8);
; template <class Epi, class Sched, bool ALIGN_EPI = false, bool SP2 = false>
; __device__ __forceinline__ void gemm_phase(PG8_LAS unsigned char* lds, const Gemm g, const Sched& S, const Epi& E, const bool skip_epi = false) {
;     ...
;             PG8_WAIT_V(8); PG8_WAIT_L(0); PG8_BAR; PG8_MMA(1, 0, At, B0); PG8_MMA(1, 1, At, B1); PG8_BAR; PG8_SCHED;
	s_setprio 1
	s_waitcnt lgkmcnt(0)
	v_mfma_f32_16x16x32_bf16 v[62:65], v[148:151], v[192:195], v[62:65]
	v_mfma_f32_16x16x32_bf16 v[58:61], v[156:159], v[192:195], v[58:61]
	v_mfma_f32_16x16x32_bf16 v[50:53], v[148:151], v[200:203], v[50:53]
	v_mfma_f32_16x16x32_bf16 v[42:45], v[156:159], v[200:203], v[42:45]
	v_mfma_f32_16x16x32_bf16 v[34:37], v[148:151], v[208:211], v[34:37]
	v_mfma_f32_16x16x32_bf16 v[26:29], v[156:159], v[208:211], v[26:29]
	v_mfma_f32_16x16x32_bf16 v[18:21], v[148:151], v[216:219], v[18:21]
	v_mfma_f32_16x16x32_bf16 v[10:13], v[156:159], v[216:219], v[10:13]
	v_mfma_f32_16x16x32_bf16 v[62:65], v[152:155], v[196:199], v[62:65]
	v_mfma_f32_16x16x32_bf16 v[58:61], v[160:163], v[196:199], v[58:61]
	v_mfma_f32_16x16x32_bf16 v[50:53], v[152:155], v[204:207], v[50:53]
	v_mfma_f32_16x16x32_bf16 v[42:45], v[160:163], v[204:207], v[42:45]
	v_mfma_f32_16x16x32_bf16 v[34:37], v[152:155], v[212:215], v[34:37]
	v_mfma_f32_16x16x32_bf16 v[26:29], v[160:163], v[212:215], v[26:29]
	v_mfma_f32_16x16x32_bf16 v[18:21], v[152:155], v[220:223], v[18:21]
	v_mfma_f32_16x16x32_bf16 v[10:13], v[160:163], v[220:223], v[10:13]
	s_setprio 0
	s_setprio 1
	v_mfma_f32_16x16x32_bf16 v[54:57], v[176:179], v[192:195], v[54:57]
	v_mfma_f32_16x16x32_bf16 v[46:49], v[184:187], v[192:195], v[46:49]
	v_mfma_f32_16x16x32_bf16 v[38:41], v[176:179], v[200:203], v[38:41]
	v_mfma_f32_16x16x32_bf16 v[30:33], v[184:187], v[200:203], v[30:33]
	v_mfma_f32_16x16x32_bf16 v[22:25], v[176:179], v[208:211], v[22:25]
	v_mfma_f32_16x16x32_bf16 v[14:17], v[184:187], v[208:211], v[14:17]
	v_mfma_f32_16x16x32_bf16 v[6:9], v[176:179], v[216:219], v[6:9]
	v_mfma_f32_16x16x32_bf16 v[2:5], v[184:187], v[216:219], v[2:5]
	v_mfma_f32_16x16x32_bf16 v[54:57], v[180:183], v[196:199], v[54:57]
	v_mfma_f32_16x16x32_bf16 v[46:49], v[188:191], v[196:199], v[46:49]
	v_mfma_f32_16x16x32_bf16 v[38:41], v[180:183], v[204:207], v[38:41]
	v_mfma_f32_16x16x32_bf16 v[30:33], v[188:191], v[204:207], v[30:33]
	v_mfma_f32_16x16x32_bf16 v[22:25], v[180:183], v[212:215], v[22:25]
	v_mfma_f32_16x16x32_bf16 v[14:17], v[188:191], v[212:215], v[14:17]
	v_mfma_f32_16x16x32_bf16 v[6:9], v[180:183], v[220:223], v[6:9]
	v_mfma_f32_16x16x32_bf16 v[2:5], v[188:191], v[220:223], v[2:5]
	s_setprio 0
	s_barrier
	s_add_i32 s60, s60, 2
	s_add_u32 s24, s24, 0x100
	s_addc_u32 s25, s25, 0
	s_add_u32 s58, s58, 0x100
	s_addc_u32 s59, s59, 0
	s_cmp_gt_u32 s60, 13
	s_cbranch_scc0 .LBB0_253
	v_lshl_add_u32 v164, s22, 8, v167
	v_ashrrev_i32_e32 v165, 31, v164
	v_lshlrev_b64 v[148:149], 6, v[164:165]
	v_lshl_add_u64 v[148:149], v[138:139], 0, v[148:149]
	v_add_co_u32_e32 v150, vcc, 0x2000, v148
	v_addc_co_u32_e32 v151, vcc, 0, v149, vcc
	global_load_dwordx4 v[176:179], v[150:151], off offset:1024
	global_load_dwordx4 v[180:183], v[150:151], off offset:2048
	global_load_dwordx4 v[184:187], v[150:151], off offset:3072
	s_and_b64 vcc, exec, s[12:13]
	s_cbranch_vccz .LBB0_256
	s_barrier
.LBB0_256:
	v_add_f32_e32 v234, v234, v235
	v_add_f32_e32 v238, v238, v239
	v_add_f32_e32 v242, v242, v243
	v_add_f32_e32 v246, v246, v247
	v_add_f32_e32 v250, v250, v251
	v_add_f32_e32 v236, v236, v237
	v_add_f32_e32 v240, v240, v241
	v_add_f32_e32 v244, v244, v245
	v_add_f32_e32 v248, v248, v249
	v_add_f32_e32 v252, v252, v253
	v_add_f32_e32 v234, v234, v236
	v_add_f32_e32 v238, v238, v240
	v_add_f32_e32 v242, v242, v244
	v_add_f32_e32 v246, v246, v248
	v_add_f32_e32 v250, v250, v252
	v_add_f32_dpp v234, v234, v234 quad_perm:[1,0,3,2] row_mask:0xf bank_mask:0xf
	v_add_f32_dpp v238, v238, v238 quad_perm:[1,0,3,2] row_mask:0xf bank_mask:0xf
	v_add_f32_dpp v242, v242, v242 quad_perm:[1,0,3,2] row_mask:0xf bank_mask:0xf
	v_add_f32_dpp v246, v246, v246 quad_perm:[1,0,3,2] row_mask:0xf bank_mask:0xf
	v_add_f32_dpp v250, v250, v250 quad_perm:[1,0,3,2] row_mask:0xf bank_mask:0xf
	v_add_f32_dpp v234, v234, v234 quad_perm:[2,3,0,1] row_mask:0xf bank_mask:0xf
	v_add_f32_dpp v238, v238, v238 quad_perm:[2,3,0,1] row_mask:0xf bank_mask:0xf
	v_add_f32_dpp v242, v242, v242 quad_perm:[2,3,0,1] row_mask:0xf bank_mask:0xf
	v_add_f32_dpp v246, v246, v246 quad_perm:[2,3,0,1] row_mask:0xf bank_mask:0xf
	v_add_f32_dpp v250, v250, v250 quad_perm:[2,3,0,1] row_mask:0xf bank_mask:0xf
	v_fmamk_f32 v234, v234, 0x3a800000, v173
	v_fmamk_f32 v238, v238, 0x3a800000, v173
	v_fmamk_f32 v242, v242, 0x3a800000, v173
	v_fmamk_f32 v246, v246, 0x3a800000, v173
	v_fmamk_f32 v250, v250, 0x3a800000, v173
	ds_bpermute_b32 v234, v168, v234
	ds_bpermute_b32 v238, v168, v238
	ds_bpermute_b32 v242, v168, v242
	ds_bpermute_b32 v246, v168, v246
	ds_bpermute_b32 v250, v168, v250
	s_cmp_eq_u32 s49, 3
	s_cselect_b64 vcc, -1, 0
	v_cndmask_b32_e32 v156, 1.0, v174, vcc
	s_cmp_lg_u32 s49, 0
	s_cselect_b64 vcc, -1, 0
	v_cndmask_b32_e32 v156, v175, v156, vcc
	v_lshl_or_b32 v208, s49, 8, v169
	v_ashrrev_i32_e32 v209, 31, v208
	v_mov_b64_e32 v[154:155], s[44:45]
	v_lshlrev_b64 v[208:209], 1, v[208:209]
	v_mad_i64_i32 v[152:153], s[24:25], v164, s48, v[154:155]
	s_nop 0
	v_lshl_add_u64 v[208:209], v[152:153], 0, v[208:209]
	s_waitcnt lgkmcnt(0)
; __device__ __forceinline__ unsigned cvt_pk_bf16(float lo, float hi) { const f32x2c_t v = {lo, hi}; return __builtin_bit_cast(unsigned, __builtin_convertvector(v, bf16x2c_t)); }
; __device__ __forceinline__ void rstd8(const float* SS, int rowb, int lane, float (&rs)[2][4]) {
;     ...
;         for (int m = 0; m < 4; ++m) { float s = (p[ai][m][0] + p[ai][m][1]) + (p[ai][m][2] + p[ai][m][3]); s += __shfl_xor(s, 1); s += __shfl_xor(s, 2);
;             const float r = __builtin_amdgcn_rsqf(s * (1.0f / 1024.0f) + RMS_EPS);
;             rs[ai][m] = __builtin_bit_cast(float, __builtin_amdgcn_ds_bpermute((lane & 15) << 4, __builtin_bit_cast(int, r))); }
;     __device__ __forceinline__ void operator()(const f32x4 (&acc)[2][2][4][2], const Unit& u, int wr, int wc, int fr, int fq) const {
;     ...
; #pragma unroll
;         for (int ai = 0; ai < 2; ++ai) {
; #pragma unroll
;             for (int m = 0; m < 4; ++m) { const float rs = rs8[ai][m] * sc;
;                 bf16_t* rowp = U + (size_t)(rowS + ai * HALF + m * 16) * ldu + colS;
; #pragma unroll
;                 for (int bj = 0; bj < 2; ++bj) { const f32x4 v0 = acc[ai][bj][m][0] * rs, v1 = acc[ai][bj][m][1] * rs;
;                     u32x4 w; w.x = cvt_pk_bf16(v0[0], v0[1]); w.y = cvt_pk_bf16(v0[2], v0[3]); w.z = cvt_pk_bf16(v1[0], v1[1]); w.w = cvt_pk_bf16(v1[2], v1[3]);
;                     *(u32x4*)(rowp + bj * HALF) = lane_perm(w, qs4); } } }
	v_rsq_f32_e32 v236, v234
	v_rsq_f32_e32 v240, v238
	v_rsq_f32_e32 v244, v242
	v_rsq_f32_e32 v248, v246
	v_rsq_f32_e32 v252, v250
	s_nop 0
	v_mul_f32_e32 v236, v156, v236
	v_mul_f32_e32 v240, v156, v240
	v_mul_f32_e32 v244, v156, v244
	v_mul_f32_e32 v248, v156, v248
	v_mul_f32_e32 v252, v156, v252
	v_pk_mul_f32 v[126:127], v[126:127], v[236:237] op_sel_hi:[1,0]
	v_pk_mul_f32 v[128:129], v[128:129], v[236:237] op_sel_hi:[1,0]
	v_pk_mul_f32 v[122:123], v[122:123], v[236:237] op_sel_hi:[1,0]
	v_pk_mul_f32 v[124:125], v[124:125], v[236:237] op_sel_hi:[1,0]
	v_pk_mul_f32 v[118:119], v[118:119], v[236:237] op_sel_hi:[1,0]
	v_pk_mul_f32 v[120:121], v[120:121], v[236:237] op_sel_hi:[1,0]
	v_pk_mul_f32 v[110:111], v[110:111], v[236:237] op_sel_hi:[1,0]
	v_pk_mul_f32 v[112:113], v[112:113], v[236:237] op_sel_hi:[1,0]
	v_cvt_pk_bf16_f32 v126, v126, v127
	v_cvt_pk_bf16_f32 v127, v128, v129
	v_cvt_pk_bf16_f32 v128, v122, v123
	v_cvt_pk_bf16_f32 v129, v124, v125
	v_cvt_pk_bf16_f32 v118, v118, v119
	v_cvt_pk_bf16_f32 v119, v120, v121
	v_cvt_pk_bf16_f32 v120, v110, v111
	v_cvt_pk_bf16_f32 v121, v112, v113
	ds_bpermute_b32 v122, v166, v126
	ds_bpermute_b32 v123, v166, v127
	ds_bpermute_b32 v124, v166, v128
	ds_bpermute_b32 v125, v166, v129
	ds_bpermute_b32 v110, v166, v118
	ds_bpermute_b32 v111, v166, v119
	ds_bpermute_b32 v112, v166, v120
	ds_bpermute_b32 v113, v166, v121
	v_mov_b32_e32 v210, v208
	v_mov_b32_e32 v211, v209
	v_pk_mul_f32 v[114:115], v[114:115], v[240:241] op_sel_hi:[1,0]
	v_pk_mul_f32 v[116:117], v[116:117], v[240:241] op_sel_hi:[1,0]
	v_pk_mul_f32 v[106:107], v[106:107], v[240:241] op_sel_hi:[1,0]
	v_pk_mul_f32 v[108:109], v[108:109], v[240:241] op_sel_hi:[1,0]
	v_pk_mul_f32 v[102:103], v[102:103], v[240:241] op_sel_hi:[1,0]
	v_pk_mul_f32 v[104:105], v[104:105], v[240:241] op_sel_hi:[1,0]
	v_pk_mul_f32 v[94:95], v[94:95], v[240:241] op_sel_hi:[1,0]
	v_pk_mul_f32 v[96:97], v[96:97], v[240:241] op_sel_hi:[1,0]
	v_cvt_pk_bf16_f32 v114, v114, v115
	v_cvt_pk_bf16_f32 v115, v116, v117
	v_cvt_pk_bf16_f32 v116, v106, v107
	v_cvt_pk_bf16_f32 v117, v108, v109
	v_cvt_pk_bf16_f32 v102, v102, v103
	v_cvt_pk_bf16_f32 v103, v104, v105
	v_cvt_pk_bf16_f32 v104, v94, v95
	v_cvt_pk_bf16_f32 v105, v96, v97
	ds_bpermute_b32 v106, v166, v114
	ds_bpermute_b32 v107, v166, v115
	ds_bpermute_b32 v108, v166, v116
	ds_bpermute_b32 v109, v166, v117
	ds_bpermute_b32 v94, v166, v102
	ds_bpermute_b32 v95, v166, v103
	ds_bpermute_b32 v96, v166, v104
	ds_bpermute_b32 v97, v166, v105
	v_add_co_u32_e32 v212, vcc, 0x18000, v208
	v_addc_co_u32_e32 v213, vcc, 0, v209, vcc
	s_waitcnt lgkmcnt(8)
	global_store_dwordx4 v[210:211], v[122:125], off
	global_store_dwordx4 v[210:211], v[110:113], off offset:256
	v_pk_mul_f32 v[98:99], v[98:99], v[244:245] op_sel_hi:[1,0]
	v_pk_mul_f32 v[100:101], v[100:101], v[244:245] op_sel_hi:[1,0]
	v_pk_mul_f32 v[90:91], v[90:91], v[244:245] op_sel_hi:[1,0]
	v_pk_mul_f32 v[92:93], v[92:93], v[244:245] op_sel_hi:[1,0]
	v_pk_mul_f32 v[86:87], v[86:87], v[244:245] op_sel_hi:[1,0]
	v_pk_mul_f32 v[88:89], v[88:89], v[244:245] op_sel_hi:[1,0]
	v_pk_mul_f32 v[78:79], v[78:79], v[244:245] op_sel_hi:[1,0]
	v_pk_mul_f32 v[80:81], v[80:81], v[244:245] op_sel_hi:[1,0]
	v_cvt_pk_bf16_f32 v98, v98, v99
	v_cvt_pk_bf16_f32 v99, v100, v101
	v_cvt_pk_bf16_f32 v100, v90, v91
	v_cvt_pk_bf16_f32 v101, v92, v93
	v_cvt_pk_bf16_f32 v86, v86, v87
	v_cvt_pk_bf16_f32 v87, v88, v89
	v_cvt_pk_bf16_f32 v88, v78, v79
	v_cvt_pk_bf16_f32 v89, v80, v81
	ds_bpermute_b32 v90, v166, v98
	ds_bpermute_b32 v91, v166, v99
	ds_bpermute_b32 v92, v166, v100
	ds_bpermute_b32 v93, v166, v101
	ds_bpermute_b32 v78, v166, v86
	ds_bpermute_b32 v79, v166, v87
	ds_bpermute_b32 v80, v166, v88
	ds_bpermute_b32 v81, v166, v89
	v_add_co_u32_e32 v210, vcc, 0x30000, v208
	v_addc_co_u32_e32 v211, vcc, 0, v209, vcc
	s_waitcnt lgkmcnt(8)
	global_store_dwordx4 v[212:213], v[106:109], off
	global_store_dwordx4 v[212:213], v[94:97], off offset:256
	v_pk_mul_f32 v[82:83], v[82:83], v[248:249] op_sel_hi:[1,0]
	v_pk_mul_f32 v[84:85], v[84:85], v[248:249] op_sel_hi:[1,0]
	v_pk_mul_f32 v[74:75], v[74:75], v[248:249] op_sel_hi:[1,0]
	v_pk_mul_f32 v[76:77], v[76:77], v[248:249] op_sel_hi:[1,0]
	v_pk_mul_f32 v[70:71], v[70:71], v[248:249] op_sel_hi:[1,0]
	v_pk_mul_f32 v[72:73], v[72:73], v[248:249] op_sel_hi:[1,0]
	v_pk_mul_f32 v[66:67], v[66:67], v[248:249] op_sel_hi:[1,0]
	v_pk_mul_f32 v[68:69], v[68:69], v[248:249] op_sel_hi:[1,0]
	v_cvt_pk_bf16_f32 v82, v82, v83
	v_cvt_pk_bf16_f32 v83, v84, v85
	v_cvt_pk_bf16_f32 v84, v74, v75
	v_cvt_pk_bf16_f32 v85, v76, v77
	v_cvt_pk_bf16_f32 v70, v70, v71
	v_cvt_pk_bf16_f32 v71, v72, v73
	v_cvt_pk_bf16_f32 v72, v66, v67
	v_cvt_pk_bf16_f32 v73, v68, v69
	ds_bpermute_b32 v74, v166, v82
	ds_bpermute_b32 v75, v166, v83
	ds_bpermute_b32 v76, v166, v84
	ds_bpermute_b32 v77, v166, v85
	ds_bpermute_b32 v66, v166, v70
	ds_bpermute_b32 v67, v166, v71
	ds_bpermute_b32 v68, v166, v72
	ds_bpermute_b32 v69, v166, v73
	v_add_co_u32_e32 v212, vcc, 0x48000, v208
	v_addc_co_u32_e32 v213, vcc, 0, v209, vcc
	s_waitcnt lgkmcnt(8)
; __device__ __forceinline__ unsigned cvt_pk_bf16(float lo, float hi) { const f32x2c_t v = {lo, hi}; return __builtin_bit_cast(unsigned, __builtin_convertvector(v, bf16x2c_t)); }
; __device__ __forceinline__ void rstd8(const float* SS, int rowb, int lane, float (&rs)[2][4]) {
;     ...
;         for (int m = 0; m < 4; ++m) { float s = (p[ai][m][0] + p[ai][m][1]) + (p[ai][m][2] + p[ai][m][3]); s += __shfl_xor(s, 1); s += __shfl_xor(s, 2);
;             const float r = __builtin_amdgcn_rsqf(s * (1.0f / 1024.0f) + RMS_EPS);
;             rs[ai][m] = __builtin_bit_cast(float, __builtin_amdgcn_ds_bpermute((lane & 15) << 4, __builtin_bit_cast(int, r))); }
;     __device__ __forceinline__ void operator()(const f32x4 (&acc)[2][2][4][2], const Unit& u, int wr, int wc, int fr, int fq) const {
;     ...
; #pragma unroll
;         for (int ai = 0; ai < 2; ++ai) {
; #pragma unroll
;             for (int m = 0; m < 4; ++m) { const float rs = rs8[ai][m] * sc;
;                 bf16_t* rowp = U + (size_t)(rowS + ai * HALF + m * 16) * ldu + colS;
; #pragma unroll
;                 for (int bj = 0; bj < 2; ++bj) { const f32x4 v0 = acc[ai][bj][m][0] * rs, v1 = acc[ai][bj][m][1] * rs;
;                     u32x4 w; w.x = cvt_pk_bf16(v0[0], v0[1]); w.y = cvt_pk_bf16(v0[2], v0[3]); w.z = cvt_pk_bf16(v1[0], v1[1]); w.w = cvt_pk_bf16(v1[2], v1[3]);
;                     *(u32x4*)(rowp + bj * HALF) = lane_perm(w, qs4); } } }
	global_store_dwordx4 v[210:211], v[90:93], off
	global_store_dwordx4 v[210:211], v[78:81], off offset:256
	v_pk_mul_f32 v[62:63], v[62:63], v[252:253] op_sel_hi:[1,0]
	v_pk_mul_f32 v[64:65], v[64:65], v[252:253] op_sel_hi:[1,0]
	v_pk_mul_f32 v[58:59], v[58:59], v[252:253] op_sel_hi:[1,0]
	v_pk_mul_f32 v[60:61], v[60:61], v[252:253] op_sel_hi:[1,0]
	v_pk_mul_f32 v[54:55], v[54:55], v[252:253] op_sel_hi:[1,0]
	v_pk_mul_f32 v[56:57], v[56:57], v[252:253] op_sel_hi:[1,0]
	v_pk_mul_f32 v[46:47], v[46:47], v[252:253] op_sel_hi:[1,0]
	v_pk_mul_f32 v[48:49], v[48:49], v[252:253] op_sel_hi:[1,0]
	v_cvt_pk_bf16_f32 v62, v62, v63
	v_cvt_pk_bf16_f32 v63, v64, v65
	v_cvt_pk_bf16_f32 v64, v58, v59
	v_cvt_pk_bf16_f32 v65, v60, v61
	v_cvt_pk_bf16_f32 v54, v54, v55
	v_cvt_pk_bf16_f32 v55, v56, v57
	v_cvt_pk_bf16_f32 v56, v46, v47
	v_cvt_pk_bf16_f32 v57, v48, v49
	ds_bpermute_b32 v58, v166, v62
	ds_bpermute_b32 v59, v166, v63
	ds_bpermute_b32 v60, v166, v64
	ds_bpermute_b32 v61, v166, v65
	ds_bpermute_b32 v46, v166, v54
	ds_bpermute_b32 v47, v166, v55
	ds_bpermute_b32 v48, v166, v56
	ds_bpermute_b32 v49, v166, v57
	v_add_co_u32_e32 v210, vcc, 0xc0000, v208
	v_addc_co_u32_e32 v211, vcc, 0, v209, vcc
	s_waitcnt lgkmcnt(8)
	global_store_dwordx4 v[212:213], v[74:77], off
	global_store_dwordx4 v[212:213], v[66:69], off offset:256
	s_waitcnt vmcnt(8)
	v_add_f32_e32 v176, v176, v177
	v_add_f32_e32 v180, v180, v181
	v_add_f32_e32 v184, v184, v185
	v_add_f32_e32 v178, v178, v179
	v_add_f32_e32 v182, v182, v183
	v_add_f32_e32 v186, v186, v187
	v_add_f32_e32 v176, v176, v178
	v_add_f32_e32 v180, v180, v182
	v_add_f32_e32 v184, v184, v186
	v_add_f32_dpp v176, v176, v176 quad_perm:[1,0,3,2] row_mask:0xf bank_mask:0xf
	v_add_f32_dpp v180, v180, v180 quad_perm:[1,0,3,2] row_mask:0xf bank_mask:0xf
	v_add_f32_dpp v184, v184, v184 quad_perm:[1,0,3,2] row_mask:0xf bank_mask:0xf
	v_add_f32_dpp v176, v176, v176 quad_perm:[2,3,0,1] row_mask:0xf bank_mask:0xf
	v_add_f32_dpp v180, v180, v180 quad_perm:[2,3,0,1] row_mask:0xf bank_mask:0xf
	v_add_f32_dpp v184, v184, v184 quad_perm:[2,3,0,1] row_mask:0xf bank_mask:0xf
	v_fmamk_f32 v176, v176, 0x3a800000, v173
	v_fmamk_f32 v180, v180, 0x3a800000, v173
	v_fmamk_f32 v184, v184, 0x3a800000, v173
	ds_bpermute_b32 v176, v168, v176
	ds_bpermute_b32 v180, v168, v180
	ds_bpermute_b32 v184, v168, v184
	s_waitcnt lgkmcnt(0)
	global_store_dwordx4 v[210:211], v[58:61], off
	global_store_dwordx4 v[210:211], v[46:49], off offset:256
	v_rsq_f32_e32 v178, v176
	v_rsq_f32_e32 v182, v180
	v_rsq_f32_e32 v186, v184
	s_nop 0
	v_mul_f32_e32 v178, v156, v178
	v_mul_f32_e32 v182, v156, v182
	v_mul_f32_e32 v186, v156, v186
	v_pk_mul_f32 v[50:51], v[50:51], v[178:179] op_sel_hi:[1,0]
	v_pk_mul_f32 v[52:53], v[52:53], v[178:179] op_sel_hi:[1,0]
	v_pk_mul_f32 v[42:43], v[42:43], v[178:179] op_sel_hi:[1,0]
	v_pk_mul_f32 v[44:45], v[44:45], v[178:179] op_sel_hi:[1,0]
	v_pk_mul_f32 v[38:39], v[38:39], v[178:179] op_sel_hi:[1,0]
	v_pk_mul_f32 v[40:41], v[40:41], v[178:179] op_sel_hi:[1,0]
	v_pk_mul_f32 v[30:31], v[30:31], v[178:179] op_sel_hi:[1,0]
	v_pk_mul_f32 v[32:33], v[32:33], v[178:179] op_sel_hi:[1,0]
	v_cvt_pk_bf16_f32 v50, v50, v51
	v_cvt_pk_bf16_f32 v51, v52, v53
	v_cvt_pk_bf16_f32 v52, v42, v43
	v_cvt_pk_bf16_f32 v53, v44, v45
	v_cvt_pk_bf16_f32 v38, v38, v39
	v_cvt_pk_bf16_f32 v39, v40, v41
	v_cvt_pk_bf16_f32 v40, v30, v31
	v_cvt_pk_bf16_f32 v41, v32, v33
	ds_bpermute_b32 v42, v166, v50
	ds_bpermute_b32 v43, v166, v51
	ds_bpermute_b32 v44, v166, v52
	ds_bpermute_b32 v45, v166, v53
	ds_bpermute_b32 v30, v166, v38
	ds_bpermute_b32 v31, v166, v39
	ds_bpermute_b32 v32, v166, v40
	ds_bpermute_b32 v33, v166, v41
	v_add_co_u32_e32 v212, vcc, 0xd8000, v208
	v_addc_co_u32_e32 v213, vcc, 0, v209, vcc
	v_pk_mul_f32 v[34:35], v[34:35], v[182:183] op_sel_hi:[1,0]
	v_pk_mul_f32 v[36:37], v[36:37], v[182:183] op_sel_hi:[1,0]
	v_pk_mul_f32 v[26:27], v[26:27], v[182:183] op_sel_hi:[1,0]
	v_pk_mul_f32 v[28:29], v[28:29], v[182:183] op_sel_hi:[1,0]
	v_pk_mul_f32 v[22:23], v[22:23], v[182:183] op_sel_hi:[1,0]
	v_pk_mul_f32 v[24:25], v[24:25], v[182:183] op_sel_hi:[1,0]
	v_pk_mul_f32 v[14:15], v[14:15], v[182:183] op_sel_hi:[1,0]
	v_pk_mul_f32 v[16:17], v[16:17], v[182:183] op_sel_hi:[1,0]
	v_cvt_pk_bf16_f32 v34, v34, v35
	v_cvt_pk_bf16_f32 v35, v36, v37
	v_cvt_pk_bf16_f32 v36, v26, v27
	v_cvt_pk_bf16_f32 v37, v28, v29
	v_cvt_pk_bf16_f32 v22, v22, v23
	v_cvt_pk_bf16_f32 v23, v24, v25
	v_cvt_pk_bf16_f32 v24, v14, v15
	v_cvt_pk_bf16_f32 v25, v16, v17
	ds_bpermute_b32 v26, v166, v34
	ds_bpermute_b32 v27, v166, v35
	ds_bpermute_b32 v28, v166, v36
	ds_bpermute_b32 v29, v166, v37
	ds_bpermute_b32 v14, v166, v22
	ds_bpermute_b32 v15, v166, v23
	ds_bpermute_b32 v16, v166, v24
	ds_bpermute_b32 v17, v166, v25
	v_add_co_u32_e32 v210, vcc, 0xf0000, v208
	v_addc_co_u32_e32 v211, vcc, 0, v209, vcc
	s_waitcnt lgkmcnt(8)
	global_store_dwordx4 v[212:213], v[42:45], off
	global_store_dwordx4 v[212:213], v[30:33], off offset:256
	v_pk_mul_f32 v[18:19], v[18:19], v[186:187] op_sel_hi:[1,0]
	v_pk_mul_f32 v[20:21], v[20:21], v[186:187] op_sel_hi:[1,0]
	v_pk_mul_f32 v[10:11], v[10:11], v[186:187] op_sel_hi:[1,0]
	v_pk_mul_f32 v[12:13], v[12:13], v[186:187] op_sel_hi:[1,0]
	v_pk_mul_f32 v[6:7], v[6:7], v[186:187] op_sel_hi:[1,0]
	v_pk_mul_f32 v[8:9], v[8:9], v[186:187] op_sel_hi:[1,0]
	v_pk_mul_f32 v[2:3], v[2:3], v[186:187] op_sel_hi:[1,0]
	v_pk_mul_f32 v[4:5], v[4:5], v[186:187] op_sel_hi:[1,0]
	v_cvt_pk_bf16_f32 v18, v18, v19
	v_cvt_pk_bf16_f32 v19, v20, v21
	v_cvt_pk_bf16_f32 v20, v10, v11
	v_cvt_pk_bf16_f32 v21, v12, v13
	v_cvt_pk_bf16_f32 v6, v6, v7
	v_cvt_pk_bf16_f32 v7, v8, v9
	v_cvt_pk_bf16_f32 v8, v2, v3
	v_cvt_pk_bf16_f32 v9, v4, v5
	ds_bpermute_b32 v10, v166, v18
	ds_bpermute_b32 v11, v166, v19
	ds_bpermute_b32 v12, v166, v20
	ds_bpermute_b32 v13, v166, v21
	ds_bpermute_b32 v2, v166, v6
	ds_bpermute_b32 v3, v166, v7
	ds_bpermute_b32 v4, v166, v8
	ds_bpermute_b32 v5, v166, v9
	v_add_co_u32_e32 v212, vcc, 0x108000, v208
	v_addc_co_u32_e32 v213, vcc, 0, v209, vcc
	s_waitcnt lgkmcnt(8)
	global_store_dwordx4 v[210:211], v[26:29], off
	global_store_dwordx4 v[210:211], v[14:17], off offset:256
	s_waitcnt lgkmcnt(0)
	global_store_dwordx4 v[212:213], v[10:13], off
	global_store_dwordx4 v[212:213], v[2:5], off offset:256
	s_andn2_b64 vcc, exec, s[4:5]
	s_mov_b64 s[4:5], -1
	s_cbranch_vccnz .LBB0_249
	s_andn2_b64 vcc, exec, s[6:7]
	s_cbranch_vccnz .LBB0_248
	s_barrier
	s_branch .LBB0_248

; #define PG8_STAGE_A(b, h, ptr, NX) do { if constexpr (Sched::GATHER) { unsigned gs_[2]; gs_[0] = ((NX) && last_) ? gN[h][0] : gA[h][0]; gs_[1] = ((NX) && last_) ? gN[h][1] : gA[h][1]; PG8_STAGE(PG8_SA(b, h), ptr, gs_); } \
;         else PG8_STAGE(PG8_SA(b, h), (ptr) + ((h) ? hstep : (size_t)0), voffA); } while (0)
; #define PG8_STAGE(bufoff, gbase, voff) do { _Pragma("unroll") for (int _i = 0; _i < 2; ++_i) \
;         __builtin_amdgcn_global_load_lds((const unsigned*)((const char*)(gbase) + (voff)[_i]), (PG8_LAS unsigned*)(lds + (bufoff) + ldsw + _i * 8192), 16, 0, 0); } while (0)
; #define PG8_LDA(dst, b, h) do { _Pragma("unroll") for (int m = 0; m < 4; ++m) _Pragma("unroll") for (int k = 0; k < 2; ++k) dst[m][k] = *(const PG8_LAS bf16x8*)(lds + PG8_SA(b, h) + aoff + m * 2048 + k * 1024); } while (0)
; #define PG8_LDB(dst, b, h) do { _Pragma("unroll") for (int n = 0; n < 2; ++n) _Pragma("unroll") for (int k = 0; k < 2; ++k) dst[n][k] = *(const PG8_LAS bf16x8*)(lds + PG8_SB(b, h) + boff + n * 2048 + k * 1024); } while (0)
; #define PG8_WAIT_V(n) asm volatile("s_waitcnt vmcnt(" #n ")" ::: "memory")
; #define PG8_WAIT_L(n) asm volatile("s_waitcnt lgkmcnt(" #n ")" ::: "memory")
; #define PG8_BAR __builtin_amdgcn_s_barrier()
; #define PG8_SCHED __builtin_amdgcn_sched_barrier(0)
; __device__ __forceinline__ void rstd8(const float* SS, int rowb, int lane, float (&rs)[2][4]) {
;     f32x4 p[2][4];
; #pragma unroll
;     for (int ai = 0; ai < 2; ++ai)
; #pragma unroll
;         for (int m = 0; m < 4; ++m) p[ai][m] = *(const f32x4*)(SS + (size_t)(rowb + HALF * ai + 16 * m + (lane >> 2)) * 16 + 4 * (lane & 3));
; template <class Epi, class Sched, bool ALIGN_EPI = false, bool SP2 = false>
; __device__ __forceinline__ void gemm_phase(PG8_LAS unsigned char* lds, const Gemm g, const Sched& S, const Epi& E, const bool skip_epi = false) {
;     ...
;             PG8_LDB(B0, 0, 0); PG8_LDB(B1, 0, 1); PG8_SCHED; PG8_LDA(At, 0, 0); PG8_STAGE_A(1, 1, a1, false);
;             PG8_WAIT_V(8); PG8_WAIT_L(0); PG8_BAR; PG8_MMA(0, 0, At, B0); PG8_MMA(0, 1, At, B1); PG8_BAR; PG8_SCHED;
;             PG8_LDA(At, 0, 1); PG8_STAGE(PG8_SB(0, 0), b2, voffB); PG8_STAGE(PG8_SB(0, 1), b2 + hstep, voffB); PG8_STAGE_A(0, 0, a2, true);
;             PG8_WAIT_V(8); PG8_WAIT_L(0); PG8_BAR; PG8_MMA(1, 0, At, B0); PG8_MMA(1, 1, At, B1); PG8_BAR; PG8_SCHED;
.LBB0_943:
	s_ashr_i32 s15, s14, 31
	s_lshl_b64 s[16:17], s[14:15], 19
	s_add_u32 s16, s86, s16
	s_addc_u32 s17, s87, s17
	s_and_b64 s[18:19], s[4:5], exec
	s_cselect_b32 s15, s17, s23
	s_cselect_b32 s54, s16, s22
	s_ashr_i32 s13, s12, 31
	s_lshl_b64 s[18:19], s[12:13], 19
	s_add_u32 s18, s2, s18
	s_addc_u32 s19, s3, s19
	s_and_b64 s[26:27], s[4:5], exec
	s_cselect_b32 s13, s19, s25
	s_cselect_b32 s55, s18, s24
	s_add_u32 s22, s22, 0x40080
	s_addc_u32 s23, s23, 0
	s_add_u32 s56, s24, 0x100
	s_addc_u32 s57, s25, 0
	s_mov_b32 s58, -2
	s_waitcnt vmcnt(0)
	v_lshl_add_u32 v148, s20, 8, v167
	v_ashrrev_i32_e32 v149, 31, v148
	v_lshlrev_b64 v[148:149], 6, v[148:149]
	v_lshl_add_u64 v[148:149], v[138:139], 0, v[148:149]
	v_add_co_u32_e32 v150, vcc, 0x2000, v148
	v_addc_co_u32_e32 v151, vcc, 0, v149, vcc
	global_load_dwordx4 v[234:237], v[148:149], off
	global_load_dwordx4 v[238:241], v[148:149], off offset:1024
	global_load_dwordx4 v[242:245], v[148:149], off offset:2048
	global_load_dwordx4 v[246:249], v[148:149], off offset:3072
	global_load_dwordx4 v[250:253], v[150:151], off
	ds_read_b128 v[148:151], v170
	ds_read_b128 v[152:155], v170 offset:1024
	ds_read_b128 v[156:159], v170 offset:2048
	ds_read_b128 v[160:163], v170 offset:3072
	ds_read_b128 v[176:179], v171
	ds_read_b128 v[180:183], v171 offset:1024
	ds_read_b128 v[184:187], v171 offset:2048
	ds_read_b128 v[188:191], v171 offset:3072
	s_add_u32 s24, s22, 0xfffc0080
	s_addc_u32 s25, s23, -1
	s_cmp_eq_u32 s58, 12
	s_cselect_b32 s27, s15, s25
	s_cselect_b32 s26, s54, s24
	s_cselect_b32 s25, s13, s57
	s_cselect_b32 s24, s55, s56
	v_lshl_add_u64 v[164:165], s[22:23], 0, v[140:141]
	s_add_i32 m0, s21, 0xc000
	ds_read_b128 v[192:195], v172
	ds_read_b128 v[196:199], v172 offset:1024
	ds_read_b128 v[200:203], v172 offset:2048
	ds_read_b128 v[204:207], v172 offset:3072
	ds_read_b128 v[208:211], v172 offset:4096
	ds_read_b128 v[212:215], v172 offset:5120
	ds_read_b128 v[216:219], v172 offset:6144
	ds_read_b128 v[220:223], v172 offset:7168
	global_load_lds_dwordx4 v[164:165], off
	v_lshl_add_u64 v[164:165], s[22:23], 0, v[142:143]
	s_add_i32 m0, s21, 0xe000
	s_nop 0
	global_load_lds_dwordx4 v[164:165], off
	s_waitcnt vmcnt(8)
	s_waitcnt lgkmcnt(0)
	s_barrier
	s_setprio 1
	s_waitcnt lgkmcnt(0)
	v_mfma_f32_16x16x32_bf16 v[126:129], v[148:151], v[192:195], 0
	v_mfma_f32_16x16x32_bf16 v[122:125], v[156:159], v[192:195], 0
	v_mfma_f32_16x16x32_bf16 v[114:117], v[148:151], v[200:203], 0
	v_mfma_f32_16x16x32_bf16 v[106:109], v[156:159], v[200:203], 0
	v_mfma_f32_16x16x32_bf16 v[98:101], v[148:151], v[208:211], 0
	v_mfma_f32_16x16x32_bf16 v[90:93], v[156:159], v[208:211], 0
	v_mfma_f32_16x16x32_bf16 v[82:85], v[148:151], v[216:219], 0
	v_mfma_f32_16x16x32_bf16 v[74:77], v[156:159], v[216:219], 0
	v_mfma_f32_16x16x32_bf16 v[126:129], v[152:155], v[196:199], v[126:129]
	v_mfma_f32_16x16x32_bf16 v[122:125], v[160:163], v[196:199], v[122:125]
	v_mfma_f32_16x16x32_bf16 v[114:117], v[152:155], v[204:207], v[114:117]
	v_mfma_f32_16x16x32_bf16 v[106:109], v[160:163], v[204:207], v[106:109]
	v_mfma_f32_16x16x32_bf16 v[98:101], v[152:155], v[212:215], v[98:101]
	v_mfma_f32_16x16x32_bf16 v[90:93], v[160:163], v[212:215], v[90:93]
	v_mfma_f32_16x16x32_bf16 v[82:85], v[152:155], v[220:223], v[82:85]
	v_mfma_f32_16x16x32_bf16 v[74:77], v[160:163], v[220:223], v[74:77]
	s_setprio 0
	s_setprio 1
	v_mfma_f32_16x16x32_bf16 v[118:121], v[176:179], v[192:195], 0
	v_mfma_f32_16x16x32_bf16 v[110:113], v[184:187], v[192:195], 0
	v_mfma_f32_16x16x32_bf16 v[102:105], v[176:179], v[200:203], 0
	v_mfma_f32_16x16x32_bf16 v[94:97], v[184:187], v[200:203], 0
	v_mfma_f32_16x16x32_bf16 v[86:89], v[176:179], v[208:211], 0
	v_mfma_f32_16x16x32_bf16 v[78:81], v[184:187], v[208:211], 0
	v_mfma_f32_16x16x32_bf16 v[70:73], v[176:179], v[216:219], 0
	v_mfma_f32_16x16x32_bf16 v[66:69], v[184:187], v[216:219], 0
	v_mfma_f32_16x16x32_bf16 v[118:121], v[180:183], v[196:199], v[118:121]
	v_mfma_f32_16x16x32_bf16 v[110:113], v[188:191], v[196:199], v[110:113]
	v_mfma_f32_16x16x32_bf16 v[102:105], v[180:183], v[204:207], v[102:105]
	v_mfma_f32_16x16x32_bf16 v[94:97], v[188:191], v[204:207], v[94:97]
	v_mfma_f32_16x16x32_bf16 v[86:89], v[180:183], v[212:215], v[86:89]
	v_mfma_f32_16x16x32_bf16 v[78:81], v[188:191], v[212:215], v[78:81]
	v_mfma_f32_16x16x32_bf16 v[70:73], v[180:183], v[220:223], v[70:73]
	v_mfma_f32_16x16x32_bf16 v[66:69], v[188:191], v[220:223], v[66:69]
	s_setprio 0
	s_barrier
	s_add_i32 s59, s48, s28
	v_lshl_add_u64 v[164:165], s[24:25], 0, v[134:135]
	s_mov_b32 m0, s59
	ds_read_b128 v[192:195], v172 offset:16384
	ds_read_b128 v[196:199], v172 offset:17408
	ds_read_b128 v[200:203], v172 offset:18432
	ds_read_b128 v[204:207], v172 offset:19456
	ds_read_b128 v[208:211], v172 offset:20480
	ds_read_b128 v[212:215], v172 offset:21504
	ds_read_b128 v[216:219], v172 offset:22528
	ds_read_b128 v[220:223], v172 offset:23552
	global_load_lds_dwordx4 v[164:165], off
	s_add_i32 m0, s59, 0x2000
	s_add_u32 s60, s24, 0x40000
	v_lshl_add_u64 v[224:225], s[24:25], 0, v[130:131]
	s_addc_u32 s61, s25, 0
	s_add_i32 s59, s49, s28
	global_load_lds_dwordx4 v[224:225], off
	v_lshl_add_u64 v[226:227], s[60:61], 0, v[134:135]
	s_mov_b32 m0, s59
	v_lshl_add_u64 v[230:231], s[26:27], 0, v[132:133]
	global_load_lds_dwordx4 v[226:227], off
	v_lshl_add_u64 v[226:227], s[60:61], 0, v[130:131]
	s_add_i32 m0, s59, 0x2000
	s_nop 0
	global_load_lds_dwordx4 v[226:227], off
	v_lshl_add_u64 v[226:227], s[26:27], 0, v[136:137]
	s_mov_b32 m0, s21
	s_nop 0
	global_load_lds_dwordx4 v[226:227], off
	s_mov_b32 m0, s31
	s_nop 0
	global_load_lds_dwordx4 v[230:231], off
	s_waitcnt vmcnt(8)
	s_waitcnt lgkmcnt(0)
	s_barrier
; #define PG8_STAGE_A(b, h, ptr, NX) do { if constexpr (Sched::GATHER) { unsigned gs_[2]; gs_[0] = ((NX) && last_) ? gN[h][0] : gA[h][0]; gs_[1] = ((NX) && last_) ? gN[h][1] : gA[h][1]; PG8_STAGE(PG8_SA(b, h), ptr, gs_); } \
;         else PG8_STAGE(PG8_SA(b, h), (ptr) + ((h) ? hstep : (size_t)0), voffA); } while (0)
; #define PG8_STAGE(bufoff, gbase, voff) do { _Pragma("unroll") for (int _i = 0; _i < 2; ++_i) \
;         __builtin_amdgcn_global_load_lds((const unsigned*)((const char*)(gbase) + (voff)[_i]), (PG8_LAS unsigned*)(lds + (bufoff) + ldsw + _i * 8192), 16, 0, 0); } while (0)
; #define PG8_LDA(dst, b, h) do { _Pragma("unroll") for (int m = 0; m < 4; ++m) _Pragma("unroll") for (int k = 0; k < 2; ++k) dst[m][k] = *(const PG8_LAS bf16x8*)(lds + PG8_SA(b, h) + aoff + m * 2048 + k * 1024); } while (0)
; #define PG8_LDB(dst, b, h) do { _Pragma("unroll") for (int n = 0; n < 2; ++n) _Pragma("unroll") for (int k = 0; k < 2; ++k) dst[n][k] = *(const PG8_LAS bf16x8*)(lds + PG8_SB(b, h) + boff + n * 2048 + k * 1024); } while (0)
; #define PG8_MMA(ai, bj, At, Bt) do { __builtin_amdgcn_s_setprio(1); _Pragma("unroll") for (int m = 0; m < 4; ++m) _Pragma("unroll") for (int n = 0; n < 2; ++n) _Pragma("unroll") for (int k = 0; k < 2; ++k) \
;         acc[ai][bj][m][n] = __builtin_amdgcn_mfma_f32_16x16x32_bf16(Bt[n][k], At[m][k], acc[ai][bj][m][n], 0, 0, 0); __builtin_amdgcn_s_setprio(0); } while (0)
; #define PG8_WAIT_V(n) asm volatile("s_waitcnt vmcnt(" #n ")" ::: "memory")
; #define PG8_WAIT_L(n) asm volatile("s_waitcnt lgkmcnt(" #n ")" ::: "memory")
; #define PG8_BAR __builtin_amdgcn_s_barrier()
; #define PG8_SCHED __builtin_amdgcn_sched_barrier(0)
; template <class Epi, class Sched, bool ALIGN_EPI = false, bool SP2 = false>
; __device__ __forceinline__ void gemm_phase(PG8_LAS unsigned char* lds, const Gemm g, const Sched& S, const Epi& E, const bool skip_epi = false) {
;     ...
;             PG8_WAIT_V(8); PG8_WAIT_L(0); PG8_BAR; PG8_MMA(1, 0, At, B0); PG8_MMA(1, 1, At, B1); PG8_BAR; PG8_SCHED;
;             PG8_LDB(B0, 1, 0); PG8_LDB(B1, 1, 1); PG8_SCHED; PG8_LDA(At, 1, 0); PG8_STAGE_A(0, 1, a2, true);
;             PG8_WAIT_V(8); PG8_WAIT_L(0); PG8_BAR; PG8_MMA(0, 0, At, B0); PG8_MMA(0, 1, At, B1); PG8_BAR; PG8_SCHED;
;             PG8_LDA(At, 1, 1); PG8_STAGE(PG8_SB(1, 0), b3, voffB); PG8_STAGE(PG8_SB(1, 1), b3 + hstep, voffB); PG8_STAGE_A(1, 0, a3, true);
	s_setprio 1
	s_waitcnt lgkmcnt(0)
	v_mfma_f32_16x16x32_bf16 v[62:65], v[148:151], v[192:195], 0
	v_mfma_f32_16x16x32_bf16 v[58:61], v[156:159], v[192:195], 0
	v_mfma_f32_16x16x32_bf16 v[50:53], v[148:151], v[200:203], 0
	v_mfma_f32_16x16x32_bf16 v[42:45], v[156:159], v[200:203], 0
	v_mfma_f32_16x16x32_bf16 v[34:37], v[148:151], v[208:211], 0
	v_mfma_f32_16x16x32_bf16 v[26:29], v[156:159], v[208:211], 0
	v_mfma_f32_16x16x32_bf16 v[18:21], v[148:151], v[216:219], 0
	v_mfma_f32_16x16x32_bf16 v[10:13], v[156:159], v[216:219], 0
	v_mfma_f32_16x16x32_bf16 v[62:65], v[152:155], v[196:199], v[62:65]
	v_mfma_f32_16x16x32_bf16 v[58:61], v[160:163], v[196:199], v[58:61]
	v_mfma_f32_16x16x32_bf16 v[50:53], v[152:155], v[204:207], v[50:53]
	v_mfma_f32_16x16x32_bf16 v[42:45], v[160:163], v[204:207], v[42:45]
	v_mfma_f32_16x16x32_bf16 v[34:37], v[152:155], v[212:215], v[34:37]
	v_mfma_f32_16x16x32_bf16 v[26:29], v[160:163], v[212:215], v[26:29]
	v_mfma_f32_16x16x32_bf16 v[18:21], v[152:155], v[220:223], v[18:21]
	v_mfma_f32_16x16x32_bf16 v[10:13], v[160:163], v[220:223], v[10:13]
	s_setprio 0
	s_setprio 1
	v_mfma_f32_16x16x32_bf16 v[54:57], v[176:179], v[192:195], 0
	v_mfma_f32_16x16x32_bf16 v[46:49], v[184:187], v[192:195], 0
	v_mfma_f32_16x16x32_bf16 v[38:41], v[176:179], v[200:203], 0
	v_mfma_f32_16x16x32_bf16 v[30:33], v[184:187], v[200:203], 0
	v_mfma_f32_16x16x32_bf16 v[22:25], v[176:179], v[208:211], 0
	v_mfma_f32_16x16x32_bf16 v[14:17], v[184:187], v[208:211], 0
	v_mfma_f32_16x16x32_bf16 v[6:9], v[176:179], v[216:219], 0
	v_mfma_f32_16x16x32_bf16 v[2:5], v[184:187], v[216:219], 0
	v_mfma_f32_16x16x32_bf16 v[54:57], v[180:183], v[196:199], v[54:57]
	v_mfma_f32_16x16x32_bf16 v[46:49], v[188:191], v[196:199], v[46:49]
	v_mfma_f32_16x16x32_bf16 v[38:41], v[180:183], v[204:207], v[38:41]
	v_mfma_f32_16x16x32_bf16 v[30:33], v[188:191], v[204:207], v[30:33]
	v_mfma_f32_16x16x32_bf16 v[22:25], v[180:183], v[212:215], v[22:25]
	v_mfma_f32_16x16x32_bf16 v[14:17], v[188:191], v[212:215], v[14:17]
	v_mfma_f32_16x16x32_bf16 v[6:9], v[180:183], v[220:223], v[6:9]
	v_mfma_f32_16x16x32_bf16 v[2:5], v[188:191], v[220:223], v[2:5]
	s_setprio 0
	s_barrier
	s_add_i32 s59, 0, 0x18000
	s_add_i32 s60, 0, 0x1c000
	v_add_u32_e32 v160, s59, v1
	v_add_u32_e32 v188, s60, v1
	ds_read_b128 v[148:151], v160
	ds_read_b128 v[152:155], v160 offset:1024
	ds_read_b128 v[156:159], v160 offset:2048
	ds_read_b128 v[160:163], v160 offset:3072
	ds_read_b128 v[176:179], v188
	ds_read_b128 v[180:183], v188 offset:1024
	ds_read_b128 v[184:187], v188 offset:2048
	ds_read_b128 v[188:191], v188 offset:3072
	s_add_u32 s26, s26, 0x40000
	s_addc_u32 s27, s27, 0
	s_mov_b32 m0, s34
	v_lshl_add_u64 v[232:233], s[26:27], 0, v[136:137]
	ds_read_b128 v[192:195], v172 offset:32768
	ds_read_b128 v[196:199], v172 offset:33792
	ds_read_b128 v[200:203], v172 offset:34816
	ds_read_b128 v[204:207], v172 offset:35840
	ds_read_b128 v[208:211], v172 offset:36864
	ds_read_b128 v[212:215], v172 offset:37888
	ds_read_b128 v[216:219], v172 offset:38912
	ds_read_b128 v[220:223], v172 offset:39936
	global_load_lds_dwordx4 v[232:233], off
	v_lshl_add_u64 v[232:233], s[26:27], 0, v[132:133]
	s_mov_b32 m0, s35
	s_nop 0
	global_load_lds_dwordx4 v[232:233], off
	s_waitcnt vmcnt(8)
	s_waitcnt lgkmcnt(0)
	s_barrier
	s_setprio 1
	s_waitcnt lgkmcnt(0)
	v_mfma_f32_16x16x32_bf16 v[126:129], v[148:151], v[192:195], v[126:129]
	v_mfma_f32_16x16x32_bf16 v[122:125], v[156:159], v[192:195], v[122:125]
	v_mfma_f32_16x16x32_bf16 v[114:117], v[148:151], v[200:203], v[114:117]
	v_mfma_f32_16x16x32_bf16 v[106:109], v[156:159], v[200:203], v[106:109]
	v_mfma_f32_16x16x32_bf16 v[98:101], v[148:151], v[208:211], v[98:101]
	v_mfma_f32_16x16x32_bf16 v[90:93], v[156:159], v[208:211], v[90:93]
	v_mfma_f32_16x16x32_bf16 v[82:85], v[148:151], v[216:219], v[82:85]
	v_mfma_f32_16x16x32_bf16 v[74:77], v[156:159], v[216:219], v[74:77]
	v_mfma_f32_16x16x32_bf16 v[126:129], v[152:155], v[196:199], v[126:129]
	v_mfma_f32_16x16x32_bf16 v[122:125], v[160:163], v[196:199], v[122:125]
	v_mfma_f32_16x16x32_bf16 v[114:117], v[152:155], v[204:207], v[114:117]
	v_mfma_f32_16x16x32_bf16 v[106:109], v[160:163], v[204:207], v[106:109]
	v_mfma_f32_16x16x32_bf16 v[98:101], v[152:155], v[212:215], v[98:101]
	v_mfma_f32_16x16x32_bf16 v[90:93], v[160:163], v[212:215], v[90:93]
	v_mfma_f32_16x16x32_bf16 v[82:85], v[152:155], v[220:223], v[82:85]
	v_mfma_f32_16x16x32_bf16 v[74:77], v[160:163], v[220:223], v[74:77]
	s_setprio 0
	s_setprio 1
	v_mfma_f32_16x16x32_bf16 v[118:121], v[176:179], v[192:195], v[118:121]
	v_mfma_f32_16x16x32_bf16 v[110:113], v[184:187], v[192:195], v[110:113]
	v_mfma_f32_16x16x32_bf16 v[102:105], v[176:179], v[200:203], v[102:105]
	v_mfma_f32_16x16x32_bf16 v[94:97], v[184:187], v[200:203], v[94:97]
	v_mfma_f32_16x16x32_bf16 v[86:89], v[176:179], v[208:211], v[86:89]
	v_mfma_f32_16x16x32_bf16 v[78:81], v[184:187], v[208:211], v[78:81]
	v_mfma_f32_16x16x32_bf16 v[70:73], v[176:179], v[216:219], v[70:73]
	v_mfma_f32_16x16x32_bf16 v[66:69], v[184:187], v[216:219], v[66:69]
	v_mfma_f32_16x16x32_bf16 v[118:121], v[180:183], v[196:199], v[118:121]
	v_mfma_f32_16x16x32_bf16 v[110:113], v[188:191], v[196:199], v[110:113]
	v_mfma_f32_16x16x32_bf16 v[102:105], v[180:183], v[204:207], v[102:105]
	v_mfma_f32_16x16x32_bf16 v[94:97], v[188:191], v[204:207], v[94:97]
	v_mfma_f32_16x16x32_bf16 v[86:89], v[180:183], v[212:215], v[86:89]
	v_mfma_f32_16x16x32_bf16 v[78:81], v[188:191], v[212:215], v[78:81]
	v_mfma_f32_16x16x32_bf16 v[70:73], v[180:183], v[220:223], v[70:73]
	v_mfma_f32_16x16x32_bf16 v[66:69], v[188:191], v[220:223], v[66:69]
	s_setprio 0
	s_barrier
; #define PG8_STAGE_A(b, h, ptr, NX) do { if constexpr (Sched::GATHER) { unsigned gs_[2]; gs_[0] = ((NX) && last_) ? gN[h][0] : gA[h][0]; gs_[1] = ((NX) && last_) ? gN[h][1] : gA[h][1]; PG8_STAGE(PG8_SA(b, h), ptr, gs_); } \
;         else PG8_STAGE(PG8_SA(b, h), (ptr) + ((h) ? hstep : (size_t)0), voffA); } while (0)
; #define PG8_STAGE(bufoff, gbase, voff) do { _Pragma("unroll") for (int _i = 0; _i < 2; ++_i) \
;         __builtin_amdgcn_global_load_lds((const unsigned*)((const char*)(gbase) + (voff)[_i]), (PG8_LAS unsigned*)(lds + (bufoff) + ldsw + _i * 8192), 16, 0, 0); } while (0)
; #define PG8_LDA(dst, b, h) do { _Pragma("unroll") for (int m = 0; m < 4; ++m) _Pragma("unroll") for (int k = 0; k < 2; ++k) dst[m][k] = *(const PG8_LAS bf16x8*)(lds + PG8_SA(b, h) + aoff + m * 2048 + k * 1024); } while (0)
; #define PG8_LDB(dst, b, h) do { _Pragma("unroll") for (int n = 0; n < 2; ++n) _Pragma("unroll") for (int k = 0; k < 2; ++k) dst[n][k] = *(const PG8_LAS bf16x8*)(lds + PG8_SB(b, h) + boff + n * 2048 + k * 1024); } while (0)
; #define PG8_MMA(ai, bj, At, Bt) do { __builtin_amdgcn_s_setprio(1); _Pragma("unroll") for (int m = 0; m < 4; ++m) _Pragma("unroll") for (int n = 0; n < 2; ++n) _Pragma("unroll") for (int k = 0; k < 2; ++k) \
;         acc[ai][bj][m][n] = __builtin_amdgcn_mfma_f32_16x16x32_bf16(Bt[n][k], At[m][k], acc[ai][bj][m][n], 0, 0, 0); __builtin_amdgcn_s_setprio(0); } while (0)
; #define PG8_WAIT_V(n) asm volatile("s_waitcnt vmcnt(" #n ")" ::: "memory")
; #define PG8_WAIT_L(n) asm volatile("s_waitcnt lgkmcnt(" #n ")" ::: "memory")
; #define PG8_BAR __builtin_amdgcn_s_barrier()
; #define PG8_SCHED __builtin_amdgcn_sched_barrier(0)
; template <class Epi, class Sched, bool ALIGN_EPI = false, bool SP2 = false>
; __device__ __forceinline__ void gemm_phase(PG8_LAS unsigned char* lds, const Gemm g, const Sched& S, const Epi& E, const bool skip_epi = false) {
;     ...
;             PG8_LDB(B0, 0, 0); PG8_LDB(B1, 0, 1); PG8_SCHED; PG8_LDA(At, 0, 0); PG8_STAGE_A(1, 1, a1, false);
;             PG8_WAIT_V(8); PG8_WAIT_L(0); PG8_BAR; PG8_MMA(0, 0, At, B0); PG8_MMA(0, 1, At, B1); PG8_BAR; PG8_SCHED;
;     ...
;             PG8_LDA(At, 1, 1); PG8_STAGE(PG8_SB(1, 0), b3, voffB); PG8_STAGE(PG8_SB(1, 1), b3 + hstep, voffB); PG8_STAGE_A(1, 0, a3, true);
;             PG8_WAIT_V(8); PG8_WAIT_L(0); PG8_BAR; PG8_MMA(1, 0, At, B0); PG8_MMA(1, 1, At, B1); PG8_BAR; PG8_SCHED;
	s_add_i32 s26, s59, s28
	v_lshl_add_u64 v[164:165], v[164:165], 0, s[8:9]
	s_mov_b32 m0, s26
	ds_read_b128 v[192:195], v172 offset:49152
	ds_read_b128 v[196:199], v172 offset:50176
	ds_read_b128 v[200:203], v172 offset:51200
	ds_read_b128 v[204:207], v172 offset:52224
	ds_read_b128 v[208:211], v172 offset:53248
	ds_read_b128 v[212:215], v172 offset:54272
	ds_read_b128 v[216:219], v172 offset:55296
	ds_read_b128 v[220:223], v172 offset:56320
	global_load_lds_dwordx4 v[164:165], off
	s_add_i32 m0, s26, 0x2000
	s_add_u32 s24, s24, 0x40080
	v_lshl_add_u64 v[164:165], v[224:225], 0, s[8:9]
	s_addc_u32 s25, s25, 0
	s_add_i32 s26, s60, s28
	global_load_lds_dwordx4 v[164:165], off
	v_lshl_add_u64 v[164:165], s[24:25], 0, v[134:135]
	s_mov_b32 m0, s26
	s_nop 0
	global_load_lds_dwordx4 v[164:165], off
	v_lshl_add_u64 v[164:165], s[24:25], 0, v[130:131]
	s_add_i32 m0, s26, 0x2000
	s_nop 0
	global_load_lds_dwordx4 v[164:165], off
	v_lshl_add_u64 v[164:165], v[226:227], 0, s[8:9]
	s_mov_b32 m0, s37
	s_nop 0
	global_load_lds_dwordx4 v[164:165], off
	v_lshl_add_u64 v[164:165], v[230:231], 0, s[8:9]
	s_mov_b32 m0, s38
	s_nop 0
	global_load_lds_dwordx4 v[164:165], off
	s_waitcnt vmcnt(8)
	s_waitcnt lgkmcnt(0)
	s_barrier
	s_setprio 1
	s_waitcnt lgkmcnt(0)
	v_mfma_f32_16x16x32_bf16 v[62:65], v[148:151], v[192:195], v[62:65]
	v_mfma_f32_16x16x32_bf16 v[58:61], v[156:159], v[192:195], v[58:61]
	v_mfma_f32_16x16x32_bf16 v[50:53], v[148:151], v[200:203], v[50:53]
	v_mfma_f32_16x16x32_bf16 v[42:45], v[156:159], v[200:203], v[42:45]
	v_mfma_f32_16x16x32_bf16 v[34:37], v[148:151], v[208:211], v[34:37]
	v_mfma_f32_16x16x32_bf16 v[26:29], v[156:159], v[208:211], v[26:29]
	v_mfma_f32_16x16x32_bf16 v[18:21], v[148:151], v[216:219], v[18:21]
	v_mfma_f32_16x16x32_bf16 v[10:13], v[156:159], v[216:219], v[10:13]
	v_mfma_f32_16x16x32_bf16 v[62:65], v[152:155], v[196:199], v[62:65]
	v_mfma_f32_16x16x32_bf16 v[58:61], v[160:163], v[196:199], v[58:61]
	v_mfma_f32_16x16x32_bf16 v[50:53], v[152:155], v[204:207], v[50:53]
	v_mfma_f32_16x16x32_bf16 v[42:45], v[160:163], v[204:207], v[42:45]
	v_mfma_f32_16x16x32_bf16 v[34:37], v[152:155], v[212:215], v[34:37]
	v_mfma_f32_16x16x32_bf16 v[26:29], v[160:163], v[212:215], v[26:29]
	v_mfma_f32_16x16x32_bf16 v[18:21], v[152:155], v[220:223], v[18:21]
	v_mfma_f32_16x16x32_bf16 v[10:13], v[160:163], v[220:223], v[10:13]
	s_setprio 0
	s_setprio 1
	v_mfma_f32_16x16x32_bf16 v[54:57], v[176:179], v[192:195], v[54:57]
	v_mfma_f32_16x16x32_bf16 v[46:49], v[184:187], v[192:195], v[46:49]
	v_mfma_f32_16x16x32_bf16 v[38:41], v[176:179], v[200:203], v[38:41]
	v_mfma_f32_16x16x32_bf16 v[30:33], v[184:187], v[200:203], v[30:33]
	v_mfma_f32_16x16x32_bf16 v[22:25], v[176:179], v[208:211], v[22:25]
	v_mfma_f32_16x16x32_bf16 v[14:17], v[184:187], v[208:211], v[14:17]
	v_mfma_f32_16x16x32_bf16 v[6:9], v[176:179], v[216:219], v[6:9]
	v_mfma_f32_16x16x32_bf16 v[2:5], v[184:187], v[216:219], v[2:5]
	v_mfma_f32_16x16x32_bf16 v[54:57], v[180:183], v[196:199], v[54:57]
	v_mfma_f32_16x16x32_bf16 v[46:49], v[188:191], v[196:199], v[46:49]
	v_mfma_f32_16x16x32_bf16 v[38:41], v[180:183], v[204:207], v[38:41]
	v_mfma_f32_16x16x32_bf16 v[30:33], v[188:191], v[204:207], v[30:33]
	v_mfma_f32_16x16x32_bf16 v[22:25], v[180:183], v[212:215], v[22:25]
	v_mfma_f32_16x16x32_bf16 v[14:17], v[188:191], v[212:215], v[14:17]
	v_mfma_f32_16x16x32_bf16 v[6:9], v[180:183], v[220:223], v[6:9]
	v_mfma_f32_16x16x32_bf16 v[2:5], v[188:191], v[220:223], v[2:5]
	s_setprio 0
	s_barrier
	s_add_i32 s58, s58, 2
	s_add_u32 s22, s22, 0x100
	s_addc_u32 s23, s23, 0
	s_add_u32 s56, s56, 0x100
	s_addc_u32 s57, s57, 0
	s_cmp_gt_u32 s58, 13
.LBB0_944:
	ds_read_b128 v[148:151], v170
	ds_read_b128 v[152:155], v170 offset:1024
	ds_read_b128 v[156:159], v170 offset:2048
	ds_read_b128 v[160:163], v170 offset:3072
	ds_read_b128 v[176:179], v171
	ds_read_b128 v[180:183], v171 offset:1024
	ds_read_b128 v[184:187], v171 offset:2048
	ds_read_b128 v[188:191], v171 offset:3072
	s_add_u32 s24, s22, 0xfffc0080
	s_addc_u32 s25, s23, -1
	s_cmp_eq_u32 s58, 12
	s_cselect_b32 s27, s15, s25
	s_cselect_b32 s26, s54, s24
	s_cselect_b32 s25, s13, s57
	s_cselect_b32 s24, s55, s56
	v_lshl_add_u64 v[164:165], s[22:23], 0, v[140:141]
	s_add_i32 m0, s21, 0xc000
	ds_read_b128 v[192:195], v172
	ds_read_b128 v[196:199], v172 offset:1024
	ds_read_b128 v[200:203], v172 offset:2048
	ds_read_b128 v[204:207], v172 offset:3072
	ds_read_b128 v[208:211], v172 offset:4096
	ds_read_b128 v[212:215], v172 offset:5120
	ds_read_b128 v[216:219], v172 offset:6144
	ds_read_b128 v[220:223], v172 offset:7168
	global_load_lds_dwordx4 v[164:165], off
	v_lshl_add_u64 v[164:165], s[22:23], 0, v[142:143]
	s_add_i32 m0, s21, 0xe000
	s_nop 0
	global_load_lds_dwordx4 v[164:165], off
	s_waitcnt vmcnt(8)
	s_waitcnt lgkmcnt(0)
	s_barrier
; #define PG8_STAGE_A(b, h, ptr, NX) do { if constexpr (Sched::GATHER) { unsigned gs_[2]; gs_[0] = ((NX) && last_) ? gN[h][0] : gA[h][0]; gs_[1] = ((NX) && last_) ? gN[h][1] : gA[h][1]; PG8_STAGE(PG8_SA(b, h), ptr, gs_); } \
;         else PG8_STAGE(PG8_SA(b, h), (ptr) + ((h) ? hstep : (size_t)0), voffA); } while (0)
; #define PG8_STAGE(bufoff, gbase, voff) do { _Pragma("unroll") for (int _i = 0; _i < 2; ++_i) \
;         __builtin_amdgcn_global_load_lds((const unsigned*)((const char*)(gbase) + (voff)[_i]), (PG8_LAS unsigned*)(lds + (bufoff) + ldsw + _i * 8192), 16, 0, 0); } while (0)
; #define PG8_LDA(dst, b, h) do { _Pragma("unroll") for (int m = 0; m < 4; ++m) _Pragma("unroll") for (int k = 0; k < 2; ++k) dst[m][k] = *(const PG8_LAS bf16x8*)(lds + PG8_SA(b, h) + aoff + m * 2048 + k * 1024); } while (0)
; #define PG8_LDB(dst, b, h) do { _Pragma("unroll") for (int n = 0; n < 2; ++n) _Pragma("unroll") for (int k = 0; k < 2; ++k) dst[n][k] = *(const PG8_LAS bf16x8*)(lds + PG8_SB(b, h) + boff + n * 2048 + k * 1024); } while (0)
; #define PG8_WAIT_V(n) asm volatile("s_waitcnt vmcnt(" #n ")" ::: "memory")
; #define PG8_BAR __builtin_amdgcn_s_barrier()
; template <class Epi, class Sched, bool ALIGN_EPI = false, bool SP2 = false>
; __device__ __forceinline__ void gemm_phase(PG8_LAS unsigned char* lds, const Gemm g, const Sched& S, const Epi& E, const bool skip_epi = false) {
;     ...
;             PG8_LDB(B0, 0, 0); PG8_LDB(B1, 0, 1); PG8_SCHED; PG8_LDA(At, 0, 0); PG8_STAGE_A(1, 1, a1, false);
;             PG8_WAIT_V(8); PG8_WAIT_L(0); PG8_BAR; PG8_MMA(0, 0, At, B0); PG8_MMA(0, 1, At, B1); PG8_BAR; PG8_SCHED;
;             PG8_LDA(At, 0, 1); PG8_STAGE(PG8_SB(0, 0), b2, voffB); PG8_STAGE(PG8_SB(0, 1), b2 + hstep, voffB); PG8_STAGE_A(0, 0, a2, true);
;             PG8_WAIT_V(8); PG8_WAIT_L(0); PG8_BAR; PG8_MMA(1, 0, At, B0); PG8_MMA(1, 1, At, B1); PG8_BAR; PG8_SCHED;
;             PG8_LDB(B0, 1, 0); PG8_LDB(B1, 1, 1); PG8_SCHED; PG8_LDA(At, 1, 0); PG8_STAGE_A(0, 1, a2, true);
;             PG8_WAIT_V(8); PG8_WAIT_L(0); PG8_BAR; PG8_MMA(0, 0, At, B0); PG8_MMA(0, 1, At, B1); PG8_BAR; PG8_SCHED;
;             PG8_LDA(At, 1, 1); PG8_STAGE(PG8_SB(1, 0), b3, voffB); PG8_STAGE(PG8_SB(1, 1), b3 + hstep, voffB); PG8_STAGE_A(1, 0, a3, true);
;             PG8_WAIT_V(8); PG8_WAIT_L(0); PG8_BAR; PG8_MMA(1, 0, At, B0); PG8_MMA(1, 1, At, B1); PG8_BAR; PG8_SCHED;
	s_setprio 1
	s_waitcnt lgkmcnt(0)
	v_mfma_f32_16x16x32_bf16 v[126:129], v[148:151], v[192:195], v[126:129]
	v_mfma_f32_16x16x32_bf16 v[122:125], v[156:159], v[192:195], v[122:125]
	v_mfma_f32_16x16x32_bf16 v[114:117], v[148:151], v[200:203], v[114:117]
	v_mfma_f32_16x16x32_bf16 v[106:109], v[156:159], v[200:203], v[106:109]
	v_mfma_f32_16x16x32_bf16 v[98:101], v[148:151], v[208:211], v[98:101]
	v_mfma_f32_16x16x32_bf16 v[90:93], v[156:159], v[208:211], v[90:93]
	v_mfma_f32_16x16x32_bf16 v[82:85], v[148:151], v[216:219], v[82:85]
	v_mfma_f32_16x16x32_bf16 v[74:77], v[156:159], v[216:219], v[74:77]
	v_mfma_f32_16x16x32_bf16 v[126:129], v[152:155], v[196:199], v[126:129]
	v_mfma_f32_16x16x32_bf16 v[122:125], v[160:163], v[196:199], v[122:125]
	v_mfma_f32_16x16x32_bf16 v[114:117], v[152:155], v[204:207], v[114:117]
	v_mfma_f32_16x16x32_bf16 v[106:109], v[160:163], v[204:207], v[106:109]
	v_mfma_f32_16x16x32_bf16 v[98:101], v[152:155], v[212:215], v[98:101]
	v_mfma_f32_16x16x32_bf16 v[90:93], v[160:163], v[212:215], v[90:93]
	v_mfma_f32_16x16x32_bf16 v[82:85], v[152:155], v[220:223], v[82:85]
	v_mfma_f32_16x16x32_bf16 v[74:77], v[160:163], v[220:223], v[74:77]
	s_setprio 0
	s_setprio 1
	v_mfma_f32_16x16x32_bf16 v[118:121], v[176:179], v[192:195], v[118:121]
	v_mfma_f32_16x16x32_bf16 v[110:113], v[184:187], v[192:195], v[110:113]
	v_mfma_f32_16x16x32_bf16 v[102:105], v[176:179], v[200:203], v[102:105]
	v_mfma_f32_16x16x32_bf16 v[94:97], v[184:187], v[200:203], v[94:97]
	v_mfma_f32_16x16x32_bf16 v[86:89], v[176:179], v[208:211], v[86:89]
	v_mfma_f32_16x16x32_bf16 v[78:81], v[184:187], v[208:211], v[78:81]
	v_mfma_f32_16x16x32_bf16 v[70:73], v[176:179], v[216:219], v[70:73]
	v_mfma_f32_16x16x32_bf16 v[66:69], v[184:187], v[216:219], v[66:69]
	v_mfma_f32_16x16x32_bf16 v[118:121], v[180:183], v[196:199], v[118:121]
	v_mfma_f32_16x16x32_bf16 v[110:113], v[188:191], v[196:199], v[110:113]
	v_mfma_f32_16x16x32_bf16 v[102:105], v[180:183], v[204:207], v[102:105]
	v_mfma_f32_16x16x32_bf16 v[94:97], v[188:191], v[204:207], v[94:97]
	v_mfma_f32_16x16x32_bf16 v[86:89], v[180:183], v[212:215], v[86:89]
	v_mfma_f32_16x16x32_bf16 v[78:81], v[188:191], v[212:215], v[78:81]
	v_mfma_f32_16x16x32_bf16 v[70:73], v[180:183], v[220:223], v[70:73]
	v_mfma_f32_16x16x32_bf16 v[66:69], v[188:191], v[220:223], v[66:69]
	s_setprio 0
	s_barrier
	s_add_i32 s59, s48, s28
	v_lshl_add_u64 v[164:165], s[24:25], 0, v[134:135]
	s_mov_b32 m0, s59
	ds_read_b128 v[192:195], v172 offset:16384
	ds_read_b128 v[196:199], v172 offset:17408
	ds_read_b128 v[200:203], v172 offset:18432
	ds_read_b128 v[204:207], v172 offset:19456
	ds_read_b128 v[208:211], v172 offset:20480
	ds_read_b128 v[212:215], v172 offset:21504
	ds_read_b128 v[216:219], v172 offset:22528
	ds_read_b128 v[220:223], v172 offset:23552
	global_load_lds_dwordx4 v[164:165], off
	s_add_i32 m0, s59, 0x2000
	s_add_u32 s60, s24, 0x40000
	v_lshl_add_u64 v[224:225], s[24:25], 0, v[130:131]
	s_addc_u32 s61, s25, 0
	s_add_i32 s59, s49, s28
	global_load_lds_dwordx4 v[224:225], off
	v_lshl_add_u64 v[226:227], s[60:61], 0, v[134:135]
	s_mov_b32 m0, s59
	v_lshl_add_u64 v[230:231], s[26:27], 0, v[132:133]
	global_load_lds_dwordx4 v[226:227], off
	v_lshl_add_u64 v[226:227], s[60:61], 0, v[130:131]
	s_add_i32 m0, s59, 0x2000
	s_nop 0
	global_load_lds_dwordx4 v[226:227], off
	v_lshl_add_u64 v[226:227], s[26:27], 0, v[136:137]
	s_mov_b32 m0, s21
	s_nop 0
	global_load_lds_dwordx4 v[226:227], off
	s_mov_b32 m0, s31
	s_nop 0
	global_load_lds_dwordx4 v[230:231], off
	s_waitcnt vmcnt(8)
	s_waitcnt lgkmcnt(0)
	s_barrier
	s_setprio 1
	s_waitcnt lgkmcnt(0)
	v_mfma_f32_16x16x32_bf16 v[62:65], v[148:151], v[192:195], v[62:65]
	v_mfma_f32_16x16x32_bf16 v[58:61], v[156:159], v[192:195], v[58:61]
	v_mfma_f32_16x16x32_bf16 v[50:53], v[148:151], v[200:203], v[50:53]
	v_mfma_f32_16x16x32_bf16 v[42:45], v[156:159], v[200:203], v[42:45]
	v_mfma_f32_16x16x32_bf16 v[34:37], v[148:151], v[208:211], v[34:37]
	v_mfma_f32_16x16x32_bf16 v[26:29], v[156:159], v[208:211], v[26:29]
	v_mfma_f32_16x16x32_bf16 v[18:21], v[148:151], v[216:219], v[18:21]
	v_mfma_f32_16x16x32_bf16 v[10:13], v[156:159], v[216:219], v[10:13]
	v_mfma_f32_16x16x32_bf16 v[62:65], v[152:155], v[196:199], v[62:65]
	v_mfma_f32_16x16x32_bf16 v[58:61], v[160:163], v[196:199], v[58:61]
	v_mfma_f32_16x16x32_bf16 v[50:53], v[152:155], v[204:207], v[50:53]
	v_mfma_f32_16x16x32_bf16 v[42:45], v[160:163], v[204:207], v[42:45]
	v_mfma_f32_16x16x32_bf16 v[34:37], v[152:155], v[212:215], v[34:37]
	v_mfma_f32_16x16x32_bf16 v[26:29], v[160:163], v[212:215], v[26:29]
	v_mfma_f32_16x16x32_bf16 v[18:21], v[152:155], v[220:223], v[18:21]
	v_mfma_f32_16x16x32_bf16 v[10:13], v[160:163], v[220:223], v[10:13]
	s_setprio 0
	s_setprio 1
	v_mfma_f32_16x16x32_bf16 v[54:57], v[176:179], v[192:195], v[54:57]
	v_mfma_f32_16x16x32_bf16 v[46:49], v[184:187], v[192:195], v[46:49]
	v_mfma_f32_16x16x32_bf16 v[38:41], v[176:179], v[200:203], v[38:41]
	v_mfma_f32_16x16x32_bf16 v[30:33], v[184:187], v[200:203], v[30:33]
	v_mfma_f32_16x16x32_bf16 v[22:25], v[176:179], v[208:211], v[22:25]
	v_mfma_f32_16x16x32_bf16 v[14:17], v[184:187], v[208:211], v[14:17]
	v_mfma_f32_16x16x32_bf16 v[6:9], v[176:179], v[216:219], v[6:9]
	v_mfma_f32_16x16x32_bf16 v[2:5], v[184:187], v[216:219], v[2:5]
	v_mfma_f32_16x16x32_bf16 v[54:57], v[180:183], v[196:199], v[54:57]
	v_mfma_f32_16x16x32_bf16 v[46:49], v[188:191], v[196:199], v[46:49]
	v_mfma_f32_16x16x32_bf16 v[38:41], v[180:183], v[204:207], v[38:41]
	v_mfma_f32_16x16x32_bf16 v[30:33], v[188:191], v[204:207], v[30:33]
	v_mfma_f32_16x16x32_bf16 v[22:25], v[180:183], v[212:215], v[22:25]
	v_mfma_f32_16x16x32_bf16 v[14:17], v[188:191], v[212:215], v[14:17]
	v_mfma_f32_16x16x32_bf16 v[6:9], v[180:183], v[220:223], v[6:9]
	v_mfma_f32_16x16x32_bf16 v[2:5], v[188:191], v[220:223], v[2:5]
	s_setprio 0
	s_barrier
; #define PG8_STAGE_A(b, h, ptr, NX) do { if constexpr (Sched::GATHER) { unsigned gs_[2]; gs_[0] = ((NX) && last_) ? gN[h][0] : gA[h][0]; gs_[1] = ((NX) && last_) ? gN[h][1] : gA[h][1]; PG8_STAGE(PG8_SA(b, h), ptr, gs_); } \
;         else PG8_STAGE(PG8_SA(b, h), (ptr) + ((h) ? hstep : (size_t)0), voffA); } while (0)
; #define PG8_STAGE(bufoff, gbase, voff) do { _Pragma("unroll") for (int _i = 0; _i < 2; ++_i) \
;         __builtin_amdgcn_global_load_lds((const unsigned*)((const char*)(gbase) + (voff)[_i]), (PG8_LAS unsigned*)(lds + (bufoff) + ldsw + _i * 8192), 16, 0, 0); } while (0)
; #define PG8_LDA(dst, b, h) do { _Pragma("unroll") for (int m = 0; m < 4; ++m) _Pragma("unroll") for (int k = 0; k < 2; ++k) dst[m][k] = *(const PG8_LAS bf16x8*)(lds + PG8_SA(b, h) + aoff + m * 2048 + k * 1024); } while (0)
; #define PG8_LDB(dst, b, h) do { _Pragma("unroll") for (int n = 0; n < 2; ++n) _Pragma("unroll") for (int k = 0; k < 2; ++k) dst[n][k] = *(const PG8_LAS bf16x8*)(lds + PG8_SB(b, h) + boff + n * 2048 + k * 1024); } while (0)
; #define PG8_WAIT_V(n) asm volatile("s_waitcnt vmcnt(" #n ")" ::: "memory")
; #define PG8_BAR __builtin_amdgcn_s_barrier()
; template <class Epi, class Sched, bool ALIGN_EPI = false, bool SP2 = false>
; __device__ __forceinline__ void gemm_phase(PG8_LAS unsigned char* lds, const Gemm g, const Sched& S, const Epi& E, const bool skip_epi = false) {
;     ...
;             PG8_LDB(B0, 0, 0); PG8_LDB(B1, 0, 1); PG8_SCHED; PG8_LDA(At, 0, 0); PG8_STAGE_A(1, 1, a1, false);
;             PG8_WAIT_V(8); PG8_WAIT_L(0); PG8_BAR; PG8_MMA(0, 0, At, B0); PG8_MMA(0, 1, At, B1); PG8_BAR; PG8_SCHED;
;             PG8_LDA(At, 0, 1); PG8_STAGE(PG8_SB(0, 0), b2, voffB); PG8_STAGE(PG8_SB(0, 1), b2 + hstep, voffB); PG8_STAGE_A(0, 0, a2, true);
;             PG8_WAIT_V(8); PG8_WAIT_L(0); PG8_BAR; PG8_MMA(1, 0, At, B0); PG8_MMA(1, 1, At, B1); PG8_BAR; PG8_SCHED;
;             PG8_LDB(B0, 1, 0); PG8_LDB(B1, 1, 1); PG8_SCHED; PG8_LDA(At, 1, 0); PG8_STAGE_A(0, 1, a2, true);
;             PG8_WAIT_V(8); PG8_WAIT_L(0); PG8_BAR; PG8_MMA(0, 0, At, B0); PG8_MMA(0, 1, At, B1); PG8_BAR; PG8_SCHED;
;             PG8_LDA(At, 1, 1); PG8_STAGE(PG8_SB(1, 0), b3, voffB); PG8_STAGE(PG8_SB(1, 1), b3 + hstep, voffB); PG8_STAGE_A(1, 0, a3, true);
;             PG8_WAIT_V(8); PG8_WAIT_L(0); PG8_BAR; PG8_MMA(1, 0, At, B0); PG8_MMA(1, 1, At, B1); PG8_BAR; PG8_SCHED;
	s_add_i32 s59, 0, 0x18000
	s_add_i32 s60, 0, 0x1c000
	v_add_u32_e32 v160, s59, v1
	v_add_u32_e32 v188, s60, v1
	ds_read_b128 v[148:151], v160
	ds_read_b128 v[152:155], v160 offset:1024
	ds_read_b128 v[156:159], v160 offset:2048
	ds_read_b128 v[160:163], v160 offset:3072
	ds_read_b128 v[176:179], v188
	ds_read_b128 v[180:183], v188 offset:1024
	ds_read_b128 v[184:187], v188 offset:2048
	ds_read_b128 v[188:191], v188 offset:3072
	s_add_u32 s26, s26, 0x40000
	s_addc_u32 s27, s27, 0
	s_mov_b32 m0, s34
	v_lshl_add_u64 v[232:233], s[26:27], 0, v[136:137]
	ds_read_b128 v[192:195], v172 offset:32768
	ds_read_b128 v[196:199], v172 offset:33792
	ds_read_b128 v[200:203], v172 offset:34816
	ds_read_b128 v[204:207], v172 offset:35840
	ds_read_b128 v[208:211], v172 offset:36864
	ds_read_b128 v[212:215], v172 offset:37888
	ds_read_b128 v[216:219], v172 offset:38912
	ds_read_b128 v[220:223], v172 offset:39936
	global_load_lds_dwordx4 v[232:233], off
	v_lshl_add_u64 v[232:233], s[26:27], 0, v[132:133]
	s_mov_b32 m0, s35
	s_nop 0
	global_load_lds_dwordx4 v[232:233], off
	s_waitcnt vmcnt(8)
	s_waitcnt lgkmcnt(0)
	s_barrier
	s_setprio 1
	s_waitcnt lgkmcnt(0)
	v_mfma_f32_16x16x32_bf16 v[126:129], v[148:151], v[192:195], v[126:129]
	v_mfma_f32_16x16x32_bf16 v[122:125], v[156:159], v[192:195], v[122:125]
	v_mfma_f32_16x16x32_bf16 v[114:117], v[148:151], v[200:203], v[114:117]
	v_mfma_f32_16x16x32_bf16 v[106:109], v[156:159], v[200:203], v[106:109]
	v_mfma_f32_16x16x32_bf16 v[98:101], v[148:151], v[208:211], v[98:101]
	v_mfma_f32_16x16x32_bf16 v[90:93], v[156:159], v[208:211], v[90:93]
	v_mfma_f32_16x16x32_bf16 v[82:85], v[148:151], v[216:219], v[82:85]
	v_mfma_f32_16x16x32_bf16 v[74:77], v[156:159], v[216:219], v[74:77]
	v_mfma_f32_16x16x32_bf16 v[126:129], v[152:155], v[196:199], v[126:129]
	v_mfma_f32_16x16x32_bf16 v[122:125], v[160:163], v[196:199], v[122:125]
	v_mfma_f32_16x16x32_bf16 v[114:117], v[152:155], v[204:207], v[114:117]
	v_mfma_f32_16x16x32_bf16 v[106:109], v[160:163], v[204:207], v[106:109]
	v_mfma_f32_16x16x32_bf16 v[98:101], v[152:155], v[212:215], v[98:101]
	v_mfma_f32_16x16x32_bf16 v[90:93], v[160:163], v[212:215], v[90:93]
	v_mfma_f32_16x16x32_bf16 v[82:85], v[152:155], v[220:223], v[82:85]
	v_mfma_f32_16x16x32_bf16 v[74:77], v[160:163], v[220:223], v[74:77]
	s_setprio 0
	s_setprio 1
	v_mfma_f32_16x16x32_bf16 v[118:121], v[176:179], v[192:195], v[118:121]
	v_mfma_f32_16x16x32_bf16 v[110:113], v[184:187], v[192:195], v[110:113]
	v_mfma_f32_16x16x32_bf16 v[102:105], v[176:179], v[200:203], v[102:105]
	v_mfma_f32_16x16x32_bf16 v[94:97], v[184:187], v[200:203], v[94:97]
	v_mfma_f32_16x16x32_bf16 v[86:89], v[176:179], v[208:211], v[86:89]
	v_mfma_f32_16x16x32_bf16 v[78:81], v[184:187], v[208:211], v[78:81]
	v_mfma_f32_16x16x32_bf16 v[70:73], v[176:179], v[216:219], v[70:73]
	v_mfma_f32_16x16x32_bf16 v[66:69], v[184:187], v[216:219], v[66:69]
	v_mfma_f32_16x16x32_bf16 v[118:121], v[180:183], v[196:199], v[118:121]
	v_mfma_f32_16x16x32_bf16 v[110:113], v[188:191], v[196:199], v[110:113]
	v_mfma_f32_16x16x32_bf16 v[102:105], v[180:183], v[204:207], v[102:105]
	v_mfma_f32_16x16x32_bf16 v[94:97], v[188:191], v[204:207], v[94:97]
	v_mfma_f32_16x16x32_bf16 v[86:89], v[180:183], v[212:215], v[86:89]
	v_mfma_f32_16x16x32_bf16 v[78:81], v[188:191], v[212:215], v[78:81]
	v_mfma_f32_16x16x32_bf16 v[70:73], v[180:183], v[220:223], v[70:73]
	v_mfma_f32_16x16x32_bf16 v[66:69], v[188:191], v[220:223], v[66:69]
	s_setprio 0
	s_barrier
	s_add_i32 s26, s59, s28
	v_lshl_add_u64 v[164:165], v[164:165], 0, s[8:9]
	s_mov_b32 m0, s26
	ds_read_b128 v[192:195], v172 offset:49152
	ds_read_b128 v[196:199], v172 offset:50176
	ds_read_b128 v[200:203], v172 offset:51200
	ds_read_b128 v[204:207], v172 offset:52224
	ds_read_b128 v[208:211], v172 offset:53248
	ds_read_b128 v[212:215], v172 offset:54272
	ds_read_b128 v[216:219], v172 offset:55296
	ds_read_b128 v[220:223], v172 offset:56320
	global_load_lds_dwordx4 v[164:165], off
	s_add_i32 m0, s26, 0x2000
	s_add_u32 s24, s24, 0x40080
	v_lshl_add_u64 v[164:165], v[224:225], 0, s[8:9]
	s_addc_u32 s25, s25, 0
	s_add_i32 s26, s60, s28
	global_load_lds_dwordx4 v[164:165], off
	v_lshl_add_u64 v[164:165], s[24:25], 0, v[134:135]
	s_mov_b32 m0, s26
	s_nop 0
	global_load_lds_dwordx4 v[164:165], off
	v_lshl_add_u64 v[164:165], s[24:25], 0, v[130:131]
	s_add_i32 m0, s26, 0x2000
	s_nop 0
	global_load_lds_dwordx4 v[164:165], off
	v_lshl_add_u64 v[164:165], v[226:227], 0, s[8:9]
	s_mov_b32 m0, s37
	s_nop 0
	global_load_lds_dwordx4 v[164:165], off
	v_lshl_add_u64 v[164:165], v[230:231], 0, s[8:9]
	s_mov_b32 m0, s38
	s_nop 0
	global_load_lds_dwordx4 v[164:165], off
	s_waitcnt vmcnt(8)
	s_waitcnt lgkmcnt(0)
	s_barrier
; #define PG8_STAGE_A(b, h, ptr, NX) do { if constexpr (Sched::GATHER) { unsigned gs_[2]; gs_[0] = ((NX) && last_) ? gN[h][0] : gA[h][0]; gs_[1] = ((NX) && last_) ? gN[h][1] : gA[h][1]; PG8_STAGE(PG8_SA(b, h), ptr, gs_); } \
;         else PG8_STAGE(PG8_SA(b, h), (ptr) + ((h) ? hstep : (size_t)0), voffA); } while (0)
; #define PG8_STAGE(bufoff, gbase, voff) do { _Pragma("unroll") for (int _i = 0; _i < 2; ++_i) \
;         __builtin_amdgcn_global_load_lds((const unsigned*)((const char*)(gbase) + (voff)[_i]), (PG8_LAS unsigned*)(lds + (bufoff) + ldsw + _i * 8192), 16, 0, 0); } while (0)
; #define PG8_WAIT_V(n) asm volatile("s_waitcnt vmcnt(" #n ")" ::: "memory")
; #define PG8_BAR __builtin_amdgcn_s_barrier()
; __device__ __forceinline__ void rstd8(const float* SS, int rowb, int lane, float (&rs)[2][4]) {
;     ...
;         for (int m = 0; m < 4; ++m) p[ai][m] = *(const f32x4*)(SS + (size_t)(rowb + HALF * ai + 16 * m + (lane >> 2)) * 16 + 4 * (lane & 3));
;     asm volatile("" : "+v"(p[0][0]), "+v"(p[0][1]), "+v"(p[0][2]), "+v"(p[0][3]), "+v"(p[1][0]), "+v"(p[1][1]), "+v"(p[1][2]), "+v"(p[1][3]));
; #pragma unroll
;     for (int ai = 0; ai < 2; ++ai)
; #pragma unroll
;         for (int m = 0; m < 4; ++m) { float s = (p[ai][m][0] + p[ai][m][1]) + (p[ai][m][2] + p[ai][m][3]); s += __shfl_xor(s, 1); s += __shfl_xor(s, 2);
;             const float r = __builtin_amdgcn_rsqf(s * (1.0f / 1024.0f) + RMS_EPS);
;             rs[ai][m] = __builtin_bit_cast(float, __builtin_amdgcn_ds_bpermute((lane & 15) << 4, __builtin_bit_cast(int, r))); }
; template <class Epi, class Sched, bool ALIGN_EPI = false, bool SP2 = false>
; __device__ __forceinline__ void gemm_phase(PG8_LAS unsigned char* lds, const Gemm g, const Sched& S, const Epi& E, const bool skip_epi = false) {
;     ...
;             PG8_WAIT_V(8); PG8_WAIT_L(0); PG8_BAR; PG8_MMA(1, 0, At, B0); PG8_MMA(1, 1, At, B1); PG8_BAR; PG8_SCHED;
;             PG8_LDB(B0, 1, 0); PG8_LDB(B1, 1, 1); PG8_SCHED; PG8_LDA(At, 1, 0); PG8_STAGE_A(0, 1, a2, true);
;             PG8_WAIT_V(8); PG8_WAIT_L(0); PG8_BAR; PG8_MMA(0, 0, At, B0); PG8_MMA(0, 1, At, B1); PG8_BAR; PG8_SCHED;
;             PG8_LDA(At, 1, 1); PG8_STAGE(PG8_SB(1, 0), b3, voffB); PG8_STAGE(PG8_SB(1, 1), b3 + hstep, voffB); PG8_STAGE_A(1, 0, a3, true);
;             PG8_WAIT_V(8); PG8_WAIT_L(0); PG8_BAR; PG8_MMA(1, 0, At, B0); PG8_MMA(1, 1, At, B1); PG8_BAR; PG8_SCHED;
	s_setprio 1
	s_waitcnt lgkmcnt(0)
	v_mfma_f32_16x16x32_bf16 v[62:65], v[148:151], v[192:195], v[62:65]
	v_mfma_f32_16x16x32_bf16 v[58:61], v[156:159], v[192:195], v[58:61]
	v_mfma_f32_16x16x32_bf16 v[50:53], v[148:151], v[200:203], v[50:53]
	v_mfma_f32_16x16x32_bf16 v[42:45], v[156:159], v[200:203], v[42:45]
	v_mfma_f32_16x16x32_bf16 v[34:37], v[148:151], v[208:211], v[34:37]
	v_mfma_f32_16x16x32_bf16 v[26:29], v[156:159], v[208:211], v[26:29]
	v_mfma_f32_16x16x32_bf16 v[18:21], v[148:151], v[216:219], v[18:21]
	v_mfma_f32_16x16x32_bf16 v[10:13], v[156:159], v[216:219], v[10:13]
	v_mfma_f32_16x16x32_bf16 v[62:65], v[152:155], v[196:199], v[62:65]
	v_mfma_f32_16x16x32_bf16 v[58:61], v[160:163], v[196:199], v[58:61]
	v_mfma_f32_16x16x32_bf16 v[50:53], v[152:155], v[204:207], v[50:53]
	v_mfma_f32_16x16x32_bf16 v[42:45], v[160:163], v[204:207], v[42:45]
	v_mfma_f32_16x16x32_bf16 v[34:37], v[152:155], v[212:215], v[34:37]
	v_mfma_f32_16x16x32_bf16 v[26:29], v[160:163], v[212:215], v[26:29]
	v_mfma_f32_16x16x32_bf16 v[18:21], v[152:155], v[220:223], v[18:21]
	v_mfma_f32_16x16x32_bf16 v[10:13], v[160:163], v[220:223], v[10:13]
	s_setprio 0
	s_setprio 1
	v_mfma_f32_16x16x32_bf16 v[54:57], v[176:179], v[192:195], v[54:57]
	v_mfma_f32_16x16x32_bf16 v[46:49], v[184:187], v[192:195], v[46:49]
	v_mfma_f32_16x16x32_bf16 v[38:41], v[176:179], v[200:203], v[38:41]
	v_mfma_f32_16x16x32_bf16 v[30:33], v[184:187], v[200:203], v[30:33]
	v_mfma_f32_16x16x32_bf16 v[22:25], v[176:179], v[208:211], v[22:25]
	v_mfma_f32_16x16x32_bf16 v[14:17], v[184:187], v[208:211], v[14:17]
	v_mfma_f32_16x16x32_bf16 v[6:9], v[176:179], v[216:219], v[6:9]
	v_mfma_f32_16x16x32_bf16 v[2:5], v[184:187], v[216:219], v[2:5]
	v_mfma_f32_16x16x32_bf16 v[54:57], v[180:183], v[196:199], v[54:57]
	v_mfma_f32_16x16x32_bf16 v[46:49], v[188:191], v[196:199], v[46:49]
	v_mfma_f32_16x16x32_bf16 v[38:41], v[180:183], v[204:207], v[38:41]
	v_mfma_f32_16x16x32_bf16 v[30:33], v[188:191], v[204:207], v[30:33]
	v_mfma_f32_16x16x32_bf16 v[22:25], v[180:183], v[212:215], v[22:25]
	v_mfma_f32_16x16x32_bf16 v[14:17], v[188:191], v[212:215], v[14:17]
	v_mfma_f32_16x16x32_bf16 v[6:9], v[180:183], v[220:223], v[6:9]
	v_mfma_f32_16x16x32_bf16 v[2:5], v[188:191], v[220:223], v[2:5]
	s_setprio 0
	s_barrier
	s_add_i32 s58, s58, 2
	s_add_u32 s22, s22, 0x100
	s_addc_u32 s23, s23, 0
	s_add_u32 s56, s56, 0x100
	s_addc_u32 s57, s57, 0
	s_cmp_gt_u32 s58, 13
	s_cbranch_scc0 .LBB0_944
	v_lshl_add_u32 v164, s20, 8, v167
	v_ashrrev_i32_e32 v165, 31, v164
	v_lshlrev_b64 v[148:149], 6, v[164:165]
	v_lshl_add_u64 v[148:149], v[138:139], 0, v[148:149]
	v_add_co_u32_e32 v150, vcc, 0x2000, v148
	v_addc_co_u32_e32 v151, vcc, 0, v149, vcc
	global_load_dwordx4 v[176:179], v[150:151], off offset:1024
	global_load_dwordx4 v[180:183], v[150:151], off offset:2048
	global_load_dwordx4 v[184:187], v[150:151], off offset:3072
	s_and_b64 vcc, exec, s[10:11]
	s_cbranch_vccz .LBB0_947
	s_barrier
.LBB0_947:
	v_add_f32_e32 v234, v234, v235
	v_add_f32_e32 v238, v238, v239
	v_add_f32_e32 v242, v242, v243
	v_add_f32_e32 v246, v246, v247
	v_add_f32_e32 v250, v250, v251
	v_add_f32_e32 v236, v236, v237
	v_add_f32_e32 v240, v240, v241
	v_add_f32_e32 v244, v244, v245
	v_add_f32_e32 v248, v248, v249
	v_add_f32_e32 v252, v252, v253
	v_add_f32_e32 v234, v234, v236
	v_add_f32_e32 v238, v238, v240
	v_add_f32_e32 v242, v242, v244
	v_add_f32_e32 v246, v246, v248
	v_add_f32_e32 v250, v250, v252
	v_add_f32_dpp v234, v234, v234 quad_perm:[1,0,3,2] row_mask:0xf bank_mask:0xf
	v_add_f32_dpp v238, v238, v238 quad_perm:[1,0,3,2] row_mask:0xf bank_mask:0xf
	v_add_f32_dpp v242, v242, v242 quad_perm:[1,0,3,2] row_mask:0xf bank_mask:0xf
	v_add_f32_dpp v246, v246, v246 quad_perm:[1,0,3,2] row_mask:0xf bank_mask:0xf
	v_add_f32_dpp v250, v250, v250 quad_perm:[1,0,3,2] row_mask:0xf bank_mask:0xf
	v_add_f32_dpp v234, v234, v234 quad_perm:[2,3,0,1] row_mask:0xf bank_mask:0xf
	v_add_f32_dpp v238, v238, v238 quad_perm:[2,3,0,1] row_mask:0xf bank_mask:0xf
	v_add_f32_dpp v242, v242, v242 quad_perm:[2,3,0,1] row_mask:0xf bank_mask:0xf
	v_add_f32_dpp v246, v246, v246 quad_perm:[2,3,0,1] row_mask:0xf bank_mask:0xf
	v_add_f32_dpp v250, v250, v250 quad_perm:[2,3,0,1] row_mask:0xf bank_mask:0xf
	v_fmamk_f32 v234, v234, 0x3a800000, v173
	v_fmamk_f32 v238, v238, 0x3a800000, v173
	v_fmamk_f32 v242, v242, 0x3a800000, v173
	v_fmamk_f32 v246, v246, 0x3a800000, v173
	v_fmamk_f32 v250, v250, 0x3a800000, v173
	ds_bpermute_b32 v234, v168, v234
	ds_bpermute_b32 v238, v168, v238
	ds_bpermute_b32 v242, v168, v242
	ds_bpermute_b32 v246, v168, v246
	ds_bpermute_b32 v250, v168, v250
	s_cmp_eq_u32 s53, 3
	s_cselect_b64 vcc, -1, 0
	v_cndmask_b32_e32 v156, 1.0, v174, vcc
	s_cmp_lg_u32 s53, 0
	s_cselect_b64 vcc, -1, 0
	v_cndmask_b32_e32 v156, v175, v156, vcc
	v_lshl_or_b32 v208, s53, 8, v169
	v_ashrrev_i32_e32 v209, 31, v208
	v_mov_b64_e32 v[154:155], s[44:45]
	v_lshlrev_b64 v[208:209], 1, v[208:209]
	v_mad_i64_i32 v[152:153], s[22:23], v164, s52, v[154:155]
	s_nop 0
	v_lshl_add_u64 v[208:209], v[152:153], 0, v[208:209]
	s_waitcnt lgkmcnt(0)
; __device__ __forceinline__ unsigned cvt_pk_bf16(float lo, float hi) { const f32x2c_t v = {lo, hi}; return __builtin_bit_cast(unsigned, __builtin_convertvector(v, bf16x2c_t)); }
; __device__ __forceinline__ void rstd8(const float* SS, int rowb, int lane, float (&rs)[2][4]) {
;     ...
;             const float r = __builtin_amdgcn_rsqf(s * (1.0f / 1024.0f) + RMS_EPS);
;             rs[ai][m] = __builtin_bit_cast(float, __builtin_amdgcn_ds_bpermute((lane & 15) << 4, __builtin_bit_cast(int, r))); }
;     __device__ __forceinline__ void operator()(const f32x4 (&acc)[2][2][4][2], const Unit& u, int wr, int wc, int fr, int fq) const {
;     ...
;             for (int m = 0; m < 4; ++m) { const float rs = rs8[ai][m] * sc;
;                 bf16_t* rowp = U + (size_t)(rowS + ai * HALF + m * 16) * ldu + colS;
; #pragma unroll
;                 for (int bj = 0; bj < 2; ++bj) { const f32x4 v0 = acc[ai][bj][m][0] * rs, v1 = acc[ai][bj][m][1] * rs;
;                     u32x4 w; w.x = cvt_pk_bf16(v0[0], v0[1]); w.y = cvt_pk_bf16(v0[2], v0[3]); w.z = cvt_pk_bf16(v1[0], v1[1]); w.w = cvt_pk_bf16(v1[2], v1[3]);
;                     *(u32x4*)(rowp + bj * HALF) = lane_perm(w, qs4); } } }
	v_rsq_f32_e32 v236, v234
	v_rsq_f32_e32 v240, v238
	v_rsq_f32_e32 v244, v242
	v_rsq_f32_e32 v248, v246
	v_rsq_f32_e32 v252, v250
	s_nop 0
	v_mul_f32_e32 v236, v156, v236
	v_mul_f32_e32 v240, v156, v240
	v_mul_f32_e32 v244, v156, v244
	v_mul_f32_e32 v248, v156, v248
	v_mul_f32_e32 v252, v156, v252
	v_pk_mul_f32 v[126:127], v[126:127], v[236:237] op_sel_hi:[1,0]
	v_pk_mul_f32 v[128:129], v[128:129], v[236:237] op_sel_hi:[1,0]
	v_pk_mul_f32 v[122:123], v[122:123], v[236:237] op_sel_hi:[1,0]
	v_pk_mul_f32 v[124:125], v[124:125], v[236:237] op_sel_hi:[1,0]
	v_pk_mul_f32 v[118:119], v[118:119], v[236:237] op_sel_hi:[1,0]
	v_pk_mul_f32 v[120:121], v[120:121], v[236:237] op_sel_hi:[1,0]
	v_pk_mul_f32 v[110:111], v[110:111], v[236:237] op_sel_hi:[1,0]
	v_pk_mul_f32 v[112:113], v[112:113], v[236:237] op_sel_hi:[1,0]
	v_cvt_pk_bf16_f32 v126, v126, v127
	v_cvt_pk_bf16_f32 v127, v128, v129
	v_cvt_pk_bf16_f32 v128, v122, v123
	v_cvt_pk_bf16_f32 v129, v124, v125
	v_cvt_pk_bf16_f32 v118, v118, v119
	v_cvt_pk_bf16_f32 v119, v120, v121
	v_cvt_pk_bf16_f32 v120, v110, v111
	v_cvt_pk_bf16_f32 v121, v112, v113
	ds_bpermute_b32 v122, v166, v126
	ds_bpermute_b32 v123, v166, v127
	ds_bpermute_b32 v124, v166, v128
	ds_bpermute_b32 v125, v166, v129
	ds_bpermute_b32 v110, v166, v118
	ds_bpermute_b32 v111, v166, v119
	ds_bpermute_b32 v112, v166, v120
	ds_bpermute_b32 v113, v166, v121
	v_mov_b32_e32 v210, v208
	v_mov_b32_e32 v211, v209
	v_pk_mul_f32 v[114:115], v[114:115], v[240:241] op_sel_hi:[1,0]
	v_pk_mul_f32 v[116:117], v[116:117], v[240:241] op_sel_hi:[1,0]
	v_pk_mul_f32 v[106:107], v[106:107], v[240:241] op_sel_hi:[1,0]
	v_pk_mul_f32 v[108:109], v[108:109], v[240:241] op_sel_hi:[1,0]
	v_pk_mul_f32 v[102:103], v[102:103], v[240:241] op_sel_hi:[1,0]
	v_pk_mul_f32 v[104:105], v[104:105], v[240:241] op_sel_hi:[1,0]
	v_pk_mul_f32 v[94:95], v[94:95], v[240:241] op_sel_hi:[1,0]
	v_pk_mul_f32 v[96:97], v[96:97], v[240:241] op_sel_hi:[1,0]
	v_cvt_pk_bf16_f32 v114, v114, v115
	v_cvt_pk_bf16_f32 v115, v116, v117
	v_cvt_pk_bf16_f32 v116, v106, v107
	v_cvt_pk_bf16_f32 v117, v108, v109
	v_cvt_pk_bf16_f32 v102, v102, v103
	v_cvt_pk_bf16_f32 v103, v104, v105
	v_cvt_pk_bf16_f32 v104, v94, v95
	v_cvt_pk_bf16_f32 v105, v96, v97
	ds_bpermute_b32 v106, v166, v114
	ds_bpermute_b32 v107, v166, v115
	ds_bpermute_b32 v108, v166, v116
	ds_bpermute_b32 v109, v166, v117
	ds_bpermute_b32 v94, v166, v102
	ds_bpermute_b32 v95, v166, v103
	ds_bpermute_b32 v96, v166, v104
	ds_bpermute_b32 v97, v166, v105
	v_add_co_u32_e32 v212, vcc, 0x18000, v208
	v_addc_co_u32_e32 v213, vcc, 0, v209, vcc
	s_waitcnt lgkmcnt(8)
	global_store_dwordx4 v[210:211], v[122:125], off
	global_store_dwordx4 v[210:211], v[110:113], off offset:256
	v_pk_mul_f32 v[98:99], v[98:99], v[244:245] op_sel_hi:[1,0]
	v_pk_mul_f32 v[100:101], v[100:101], v[244:245] op_sel_hi:[1,0]
	v_pk_mul_f32 v[90:91], v[90:91], v[244:245] op_sel_hi:[1,0]
	v_pk_mul_f32 v[92:93], v[92:93], v[244:245] op_sel_hi:[1,0]
	v_pk_mul_f32 v[86:87], v[86:87], v[244:245] op_sel_hi:[1,0]
	v_pk_mul_f32 v[88:89], v[88:89], v[244:245] op_sel_hi:[1,0]
	v_pk_mul_f32 v[78:79], v[78:79], v[244:245] op_sel_hi:[1,0]
	v_pk_mul_f32 v[80:81], v[80:81], v[244:245] op_sel_hi:[1,0]
	v_cvt_pk_bf16_f32 v98, v98, v99
	v_cvt_pk_bf16_f32 v99, v100, v101
	v_cvt_pk_bf16_f32 v100, v90, v91
	v_cvt_pk_bf16_f32 v101, v92, v93
	v_cvt_pk_bf16_f32 v86, v86, v87
	v_cvt_pk_bf16_f32 v87, v88, v89
	v_cvt_pk_bf16_f32 v88, v78, v79
	v_cvt_pk_bf16_f32 v89, v80, v81
	ds_bpermute_b32 v90, v166, v98
	ds_bpermute_b32 v91, v166, v99
	ds_bpermute_b32 v92, v166, v100
	ds_bpermute_b32 v93, v166, v101
	ds_bpermute_b32 v78, v166, v86
	ds_bpermute_b32 v79, v166, v87
	ds_bpermute_b32 v80, v166, v88
	ds_bpermute_b32 v81, v166, v89
	v_add_co_u32_e32 v210, vcc, 0x30000, v208
	v_addc_co_u32_e32 v211, vcc, 0, v209, vcc
	s_waitcnt lgkmcnt(8)
	global_store_dwordx4 v[212:213], v[106:109], off
	global_store_dwordx4 v[212:213], v[94:97], off offset:256
	v_pk_mul_f32 v[82:83], v[82:83], v[248:249] op_sel_hi:[1,0]
	v_pk_mul_f32 v[84:85], v[84:85], v[248:249] op_sel_hi:[1,0]
	v_pk_mul_f32 v[74:75], v[74:75], v[248:249] op_sel_hi:[1,0]
	v_pk_mul_f32 v[76:77], v[76:77], v[248:249] op_sel_hi:[1,0]
	v_pk_mul_f32 v[70:71], v[70:71], v[248:249] op_sel_hi:[1,0]
	v_pk_mul_f32 v[72:73], v[72:73], v[248:249] op_sel_hi:[1,0]
	v_pk_mul_f32 v[66:67], v[66:67], v[248:249] op_sel_hi:[1,0]
	v_pk_mul_f32 v[68:69], v[68:69], v[248:249] op_sel_hi:[1,0]
	v_cvt_pk_bf16_f32 v82, v82, v83
	v_cvt_pk_bf16_f32 v83, v84, v85
	v_cvt_pk_bf16_f32 v84, v74, v75
	v_cvt_pk_bf16_f32 v85, v76, v77
	v_cvt_pk_bf16_f32 v70, v70, v71
	v_cvt_pk_bf16_f32 v71, v72, v73
	v_cvt_pk_bf16_f32 v72, v66, v67
	v_cvt_pk_bf16_f32 v73, v68, v69
	ds_bpermute_b32 v74, v166, v82
	ds_bpermute_b32 v75, v166, v83
	ds_bpermute_b32 v76, v166, v84
	ds_bpermute_b32 v77, v166, v85
	ds_bpermute_b32 v66, v166, v70
	ds_bpermute_b32 v67, v166, v71
	ds_bpermute_b32 v68, v166, v72
	ds_bpermute_b32 v69, v166, v73
	v_add_co_u32_e32 v212, vcc, 0x48000, v208
	v_addc_co_u32_e32 v213, vcc, 0, v209, vcc
	s_waitcnt lgkmcnt(8)
; __device__ __forceinline__ unsigned cvt_pk_bf16(float lo, float hi) { const f32x2c_t v = {lo, hi}; return __builtin_bit_cast(unsigned, __builtin_convertvector(v, bf16x2c_t)); }
; __device__ __forceinline__ void rstd8(const float* SS, int rowb, int lane, float (&rs)[2][4]) {
;     ...
;         for (int m = 0; m < 4; ++m) p[ai][m] = *(const f32x4*)(SS + (size_t)(rowb + HALF * ai + 16 * m + (lane >> 2)) * 16 + 4 * (lane & 3));
;     asm volatile("" : "+v"(p[0][0]), "+v"(p[0][1]), "+v"(p[0][2]), "+v"(p[0][3]), "+v"(p[1][0]), "+v"(p[1][1]), "+v"(p[1][2]), "+v"(p[1][3]));
; #pragma unroll
;     for (int ai = 0; ai < 2; ++ai)
; #pragma unroll
;         for (int m = 0; m < 4; ++m) { float s = (p[ai][m][0] + p[ai][m][1]) + (p[ai][m][2] + p[ai][m][3]); s += __shfl_xor(s, 1); s += __shfl_xor(s, 2);
;             const float r = __builtin_amdgcn_rsqf(s * (1.0f / 1024.0f) + RMS_EPS);
;             rs[ai][m] = __builtin_bit_cast(float, __builtin_amdgcn_ds_bpermute((lane & 15) << 4, __builtin_bit_cast(int, r))); }
;     __device__ __forceinline__ void operator()(const f32x4 (&acc)[2][2][4][2], const Unit& u, int wr, int wc, int fr, int fq) const {
;     ...
;             for (int m = 0; m < 4; ++m) { const float rs = rs8[ai][m] * sc;
;                 bf16_t* rowp = U + (size_t)(rowS + ai * HALF + m * 16) * ldu + colS;
; #pragma unroll
;                 for (int bj = 0; bj < 2; ++bj) { const f32x4 v0 = acc[ai][bj][m][0] * rs, v1 = acc[ai][bj][m][1] * rs;
;                     u32x4 w; w.x = cvt_pk_bf16(v0[0], v0[1]); w.y = cvt_pk_bf16(v0[2], v0[3]); w.z = cvt_pk_bf16(v1[0], v1[1]); w.w = cvt_pk_bf16(v1[2], v1[3]);
;                     *(u32x4*)(rowp + bj * HALF) = lane_perm(w, qs4); } } }
	global_store_dwordx4 v[210:211], v[90:93], off
	global_store_dwordx4 v[210:211], v[78:81], off offset:256
	v_pk_mul_f32 v[62:63], v[62:63], v[252:253] op_sel_hi:[1,0]
	v_pk_mul_f32 v[64:65], v[64:65], v[252:253] op_sel_hi:[1,0]
	v_pk_mul_f32 v[58:59], v[58:59], v[252:253] op_sel_hi:[1,0]
	v_pk_mul_f32 v[60:61], v[60:61], v[252:253] op_sel_hi:[1,0]
	v_pk_mul_f32 v[54:55], v[54:55], v[252:253] op_sel_hi:[1,0]
	v_pk_mul_f32 v[56:57], v[56:57], v[252:253] op_sel_hi:[1,0]
	v_pk_mul_f32 v[46:47], v[46:47], v[252:253] op_sel_hi:[1,0]
	v_pk_mul_f32 v[48:49], v[48:49], v[252:253] op_sel_hi:[1,0]
	v_cvt_pk_bf16_f32 v62, v62, v63
	v_cvt_pk_bf16_f32 v63, v64, v65
	v_cvt_pk_bf16_f32 v64, v58, v59
	v_cvt_pk_bf16_f32 v65, v60, v61
	v_cvt_pk_bf16_f32 v54, v54, v55
	v_cvt_pk_bf16_f32 v55, v56, v57
	v_cvt_pk_bf16_f32 v56, v46, v47
	v_cvt_pk_bf16_f32 v57, v48, v49
	ds_bpermute_b32 v58, v166, v62
	ds_bpermute_b32 v59, v166, v63
	ds_bpermute_b32 v60, v166, v64
	ds_bpermute_b32 v61, v166, v65
	ds_bpermute_b32 v46, v166, v54
	ds_bpermute_b32 v47, v166, v55
	ds_bpermute_b32 v48, v166, v56
	ds_bpermute_b32 v49, v166, v57
	v_add_co_u32_e32 v210, vcc, 0xc0000, v208
	v_addc_co_u32_e32 v211, vcc, 0, v209, vcc
	s_waitcnt lgkmcnt(8)
	global_store_dwordx4 v[212:213], v[74:77], off
	global_store_dwordx4 v[212:213], v[66:69], off offset:256
	s_waitcnt vmcnt(8)
	v_add_f32_e32 v176, v176, v177
	v_add_f32_e32 v180, v180, v181
	v_add_f32_e32 v184, v184, v185
	v_add_f32_e32 v178, v178, v179
	v_add_f32_e32 v182, v182, v183
	v_add_f32_e32 v186, v186, v187
	v_add_f32_e32 v176, v176, v178
	v_add_f32_e32 v180, v180, v182
	v_add_f32_e32 v184, v184, v186
	v_add_f32_dpp v176, v176, v176 quad_perm:[1,0,3,2] row_mask:0xf bank_mask:0xf
	v_add_f32_dpp v180, v180, v180 quad_perm:[1,0,3,2] row_mask:0xf bank_mask:0xf
	v_add_f32_dpp v184, v184, v184 quad_perm:[1,0,3,2] row_mask:0xf bank_mask:0xf
	v_add_f32_dpp v176, v176, v176 quad_perm:[2,3,0,1] row_mask:0xf bank_mask:0xf
	v_add_f32_dpp v180, v180, v180 quad_perm:[2,3,0,1] row_mask:0xf bank_mask:0xf
	v_add_f32_dpp v184, v184, v184 quad_perm:[2,3,0,1] row_mask:0xf bank_mask:0xf
	v_fmamk_f32 v176, v176, 0x3a800000, v173
	v_fmamk_f32 v180, v180, 0x3a800000, v173
	v_fmamk_f32 v184, v184, 0x3a800000, v173
	ds_bpermute_b32 v176, v168, v176
	ds_bpermute_b32 v180, v168, v180
	ds_bpermute_b32 v184, v168, v184
	s_waitcnt lgkmcnt(0)
	global_store_dwordx4 v[210:211], v[58:61], off
	global_store_dwordx4 v[210:211], v[46:49], off offset:256
	v_rsq_f32_e32 v178, v176
	v_rsq_f32_e32 v182, v180
	v_rsq_f32_e32 v186, v184
	s_nop 0
	v_mul_f32_e32 v178, v156, v178
	v_mul_f32_e32 v182, v156, v182
	v_mul_f32_e32 v186, v156, v186
	v_pk_mul_f32 v[50:51], v[50:51], v[178:179] op_sel_hi:[1,0]
	v_pk_mul_f32 v[52:53], v[52:53], v[178:179] op_sel_hi:[1,0]
	v_pk_mul_f32 v[42:43], v[42:43], v[178:179] op_sel_hi:[1,0]
	v_pk_mul_f32 v[44:45], v[44:45], v[178:179] op_sel_hi:[1,0]
	v_pk_mul_f32 v[38:39], v[38:39], v[178:179] op_sel_hi:[1,0]
	v_pk_mul_f32 v[40:41], v[40:41], v[178:179] op_sel_hi:[1,0]
	v_pk_mul_f32 v[30:31], v[30:31], v[178:179] op_sel_hi:[1,0]
	v_pk_mul_f32 v[32:33], v[32:33], v[178:179] op_sel_hi:[1,0]
	v_cvt_pk_bf16_f32 v50, v50, v51
	v_cvt_pk_bf16_f32 v51, v52, v53
	v_cvt_pk_bf16_f32 v52, v42, v43
	v_cvt_pk_bf16_f32 v53, v44, v45
	v_cvt_pk_bf16_f32 v38, v38, v39
	v_cvt_pk_bf16_f32 v39, v40, v41
	v_cvt_pk_bf16_f32 v40, v30, v31
	v_cvt_pk_bf16_f32 v41, v32, v33
	ds_bpermute_b32 v42, v166, v50
	ds_bpermute_b32 v43, v166, v51
	ds_bpermute_b32 v44, v166, v52
	ds_bpermute_b32 v45, v166, v53
	ds_bpermute_b32 v30, v166, v38
	ds_bpermute_b32 v31, v166, v39
	ds_bpermute_b32 v32, v166, v40
	ds_bpermute_b32 v33, v166, v41
	v_add_co_u32_e32 v212, vcc, 0xd8000, v208
	v_addc_co_u32_e32 v213, vcc, 0, v209, vcc
	v_pk_mul_f32 v[34:35], v[34:35], v[182:183] op_sel_hi:[1,0]
	v_pk_mul_f32 v[36:37], v[36:37], v[182:183] op_sel_hi:[1,0]
	v_pk_mul_f32 v[26:27], v[26:27], v[182:183] op_sel_hi:[1,0]
	v_pk_mul_f32 v[28:29], v[28:29], v[182:183] op_sel_hi:[1,0]
	v_pk_mul_f32 v[22:23], v[22:23], v[182:183] op_sel_hi:[1,0]
	v_pk_mul_f32 v[24:25], v[24:25], v[182:183] op_sel_hi:[1,0]
	v_pk_mul_f32 v[14:15], v[14:15], v[182:183] op_sel_hi:[1,0]
	v_pk_mul_f32 v[16:17], v[16:17], v[182:183] op_sel_hi:[1,0]
	v_cvt_pk_bf16_f32 v34, v34, v35
	v_cvt_pk_bf16_f32 v35, v36, v37
	v_cvt_pk_bf16_f32 v36, v26, v27
	v_cvt_pk_bf16_f32 v37, v28, v29
	v_cvt_pk_bf16_f32 v22, v22, v23
	v_cvt_pk_bf16_f32 v23, v24, v25
	v_cvt_pk_bf16_f32 v24, v14, v15
	v_cvt_pk_bf16_f32 v25, v16, v17
	ds_bpermute_b32 v26, v166, v34
	ds_bpermute_b32 v27, v166, v35
	ds_bpermute_b32 v28, v166, v36
	ds_bpermute_b32 v29, v166, v37
	ds_bpermute_b32 v14, v166, v22
	ds_bpermute_b32 v15, v166, v23
	ds_bpermute_b32 v16, v166, v24
	ds_bpermute_b32 v17, v166, v25
	v_add_co_u32_e32 v210, vcc, 0xf0000, v208
	v_addc_co_u32_e32 v211, vcc, 0, v209, vcc
	s_waitcnt lgkmcnt(8)
	global_store_dwordx4 v[212:213], v[42:45], off
	global_store_dwordx4 v[212:213], v[30:33], off offset:256
	v_pk_mul_f32 v[18:19], v[18:19], v[186:187] op_sel_hi:[1,0]
	v_pk_mul_f32 v[20:21], v[20:21], v[186:187] op_sel_hi:[1,0]
	v_pk_mul_f32 v[10:11], v[10:11], v[186:187] op_sel_hi:[1,0]
	v_pk_mul_f32 v[12:13], v[12:13], v[186:187] op_sel_hi:[1,0]
	v_pk_mul_f32 v[6:7], v[6:7], v[186:187] op_sel_hi:[1,0]
	v_pk_mul_f32 v[8:9], v[8:9], v[186:187] op_sel_hi:[1,0]
	v_pk_mul_f32 v[2:3], v[2:3], v[186:187] op_sel_hi:[1,0]
	v_pk_mul_f32 v[4:5], v[4:5], v[186:187] op_sel_hi:[1,0]
	v_cvt_pk_bf16_f32 v18, v18, v19
	v_cvt_pk_bf16_f32 v19, v20, v21
	v_cvt_pk_bf16_f32 v20, v10, v11
	v_cvt_pk_bf16_f32 v21, v12, v13
	v_cvt_pk_bf16_f32 v6, v6, v7
	v_cvt_pk_bf16_f32 v7, v8, v9
	v_cvt_pk_bf16_f32 v8, v2, v3
	v_cvt_pk_bf16_f32 v9, v4, v5
	ds_bpermute_b32 v10, v166, v18
	ds_bpermute_b32 v11, v166, v19
	ds_bpermute_b32 v12, v166, v20
	ds_bpermute_b32 v13, v166, v21
	ds_bpermute_b32 v2, v166, v6
	ds_bpermute_b32 v3, v166, v7
	ds_bpermute_b32 v4, v166, v8
	ds_bpermute_b32 v5, v166, v9
	v_add_co_u32_e32 v212, vcc, 0x108000, v208
	v_addc_co_u32_e32 v213, vcc, 0, v209, vcc
	s_waitcnt lgkmcnt(8)
	global_store_dwordx4 v[210:211], v[26:29], off
	global_store_dwordx4 v[210:211], v[14:17], off offset:256
	s_waitcnt lgkmcnt(0)
	global_store_dwordx4 v[212:213], v[10:13], off
	global_store_dwordx4 v[212:213], v[2:5], off offset:256
	s_andn2_b64 vcc, exec, s[4:5]
	s_mov_b64 s[4:5], -1
	s_cbranch_vccnz .LBB0_940
	s_andn2_b64 vcc, exec, s[6:7]
	s_cbranch_vccnz .LBB0_939
	s_barrier
	s_branch .LBB0_939
